# MoE epilogues: one wait for all loads before the first exec-masked row group, per-row-group and back-edge vmcnt waits (which drained the stores) removed; P9 next-unit row-list loads consumed in the K-
# baseline (speedup 1.0000x reference)
.LBB0_1151:
	s_andn2_b64 vcc, exec, s[2:3]
	v_mov_b32_e32 v132, v175
	v_mov_b32_e32 v131, v174
	v_mov_b32_e32 v130, v173
	v_mov_b32_e32 v129, v147
	s_mov_b32 s39, s64
	s_mov_b32 s38, s63
	s_mov_b32 s65, s62
	v_mov_b32_e32 v128, v146
	s_mov_b32 s66, s23
	s_cbranch_vccz .LBB0_1179

.LBB0_1154:
	v_cndmask_b32_e64 v133, 0, 1, s[10:11]
	v_cmp_ne_u32_e64 s[2:3], 1, v133
	s_andn2_b64 vcc, exec, s[10:11]
	v_mov_b32_e32 v175, v132
	v_mov_b32_e32 v174, v131
	v_mov_b32_e32 v173, v130
	v_mov_b32_e32 v147, v129
	s_mov_b32 s23, s66
	s_cbranch_vccnz .LBB0_1156
	v_ashrrev_i32_e32 v147, 31, v146
	s_add_i32 s67, s63, -1
	s_ashr_i32 s23, s22, 31
	v_lshlrev_b64 v[136:137], 18, v[146:147]
	v_min_i32_e32 v134, s67, v152
	v_lshl_add_u64 v[136:137], s[12:13], 0, v[136:137]
	s_lshl_b64 s[10:11], s[22:23], 2
	v_min_i32_e32 v138, s67, v153
	v_min_i32_e32 v140, s67, v154
	v_min_i32_e32 v142, s67, v155
	v_ashrrev_i32_e32 v135, 31, v134
	v_lshl_add_u64 v[136:137], v[136:137], 0, s[10:11]
	v_ashrrev_i32_e32 v139, 31, v138
	v_ashrrev_i32_e32 v141, 31, v140
	v_ashrrev_i32_e32 v143, 31, v142
	v_lshl_add_u64 v[134:135], v[134:135], 2, v[136:137]
	v_lshl_add_u64 v[138:139], v[138:139], 2, v[136:137]
	v_lshl_add_u64 v[140:141], v[140:141], 2, v[136:137]
	v_lshl_add_u64 v[136:137], v[142:143], 2, v[136:137]
	global_load_dword v147, v[134:135], off
	s_nop 0
	global_load_dword v173, v[138:139], off
	global_load_dword v174, v[140:141], off
	s_nop 0
	global_load_dword v175, v[136:137], off
	v_lshlrev_b32_e32 v137, 22, v146
	s_lshl_b32 s10, s62, 18
	v_add_u32_e32 v137, s10, v137
	s_nop 0
	v_readfirstlane_b32 s10, v137
	s_lshl_b32 s23, s10, 1

.LBB0_1157:
	s_cmp_lg_u32 s67, 10
	s_cbranch_scc1 .Lp9_na_done
	s_and_b64 vcc, exec, s[2:3]
	s_cbranch_vccnz .Lp9_na_done
	v_lshlrev_b32_e32 v147, 8, v147
	v_lshlrev_b32_e32 v173, 8, v173
	v_lshlrev_b32_e32 v174, 8, v174
	v_lshlrev_b32_e32 v175, 8, v175
	v_and_b32_e32 v147, 0x7ffffc00, v147
	v_and_b32_e32 v173, 0x7ffffc00, v173
	v_and_b32_e32 v174, 0x7ffffc00, v174
	v_and_b32_e32 v175, 0x7ffffc00, v175
	v_add_lshl_u32 v147, v147, v156, 1
	v_add_lshl_u32 v173, v173, v158, 1
	v_add_lshl_u32 v174, v174, v156, 1
	v_add_lshl_u32 v175, v175, v158, 1

.LBB0_1160:
	v_ashrrev_i32_e32 v129, 31, v128
	v_lshl_or_b32 v148, s65, 8, v161
	v_lshlrev_b64 v[128:129], 14, v[128:129]
	v_lshl_add_u64 v[128:129], s[72:73], 0, v[128:129]
	v_ashrrev_i32_e32 v149, 31, v148
	s_nop 15
	s_nop 15
	v_lshl_add_u64 v[132:133], v[148:149], 2, v[128:129]
	global_load_dwordx4 v[136:139], v[132:133], off offset:16
	global_load_dwordx4 v[140:143], v[132:133], off
	global_load_dwordx4 v[128:131], v[132:133], off offset:528
	s_nop 0
	global_load_dwordx4 v[132:135], v[132:133], off offset:512
	v_add_u32_e32 v144, s39, v160
	v_cmp_gt_i32_e32 vcc, s38, v160
	v_ashrrev_i32_e32 v150, 1, v148
	v_add_u32_e32 v148, 0x80, v148
	v_cndmask_b32_e32 v144, -1, v144, vcc
	v_cmp_lt_i32_e32 vcc, -1, v144
	v_ashrrev_i32_e32 v151, 31, v150
	v_ashrrev_i32_e32 v148, 1, v148
	s_waitcnt vmcnt(0)
	s_and_saveexec_b64 s[10:11], vcc
	s_cbranch_execz .LBB0_1162
	v_pk_fma_f32 v[124:125], v[124:125], s[20:21], v[140:141] op_sel_hi:[1,0,1]
	v_lshlrev_b64 v[176:177], 11, v[144:145]
	v_min_f32_e32 v124, 0x40e00000, v124
	v_mul_f32_e32 v144, 0x3fd9db23, v124
	v_mul_f32_e32 v144, 0xbfb8aa3b, v144
	v_exp_f32_e32 v144, v144
	v_pk_fma_f32 v[126:127], v[126:127], s[20:21], v[142:143] op_sel_hi:[1,0,1]
	v_pk_fma_f32 v[120:121], v[120:121], s[20:21], v[136:137] op_sel_hi:[1,0,1]
	v_min_f32_e32 v126, 0x40e00000, v126
	v_add_f32_e32 v144, 1.0, v144
	v_mul_f32_e32 v149, 0x3fd9db23, v126
	v_rcp_f32_e32 v144, v144
	v_mul_f32_e32 v149, 0xbfb8aa3b, v149
	v_exp_f32_e32 v149, v149
	v_med3_f32 v125, v125, s61, v172
	v_mul_f32_e32 v124, v124, v144
	v_add_f32_e32 v125, 1.0, v125
	v_min_f32_e32 v120, 0x40e00000, v120
	v_add_f32_e32 v144, 1.0, v149
	v_mul_f32_e32 v124, v125, v124
	v_med3_f32 v125, v127, s61, v172
	v_mul_f32_e32 v127, 0x3fd9db23, v120
	v_rcp_f32_e32 v144, v144
	v_mul_f32_e32 v127, 0xbfb8aa3b, v127
	v_exp_f32_e32 v127, v127
	v_pk_fma_f32 v[122:123], v[122:123], s[20:21], v[138:139] op_sel_hi:[1,0,1]
	v_mul_f32_e32 v126, v126, v144
	v_add_f32_e32 v125, 1.0, v125
	v_min_f32_e32 v122, 0x40e00000, v122
	v_mul_f32_e32 v125, v125, v126
	v_add_f32_e32 v126, 1.0, v127
	v_mul_f32_e32 v127, 0x3fd9db23, v122
	v_rcp_f32_e32 v126, v126
	v_mul_f32_e32 v127, 0xbfb8aa3b, v127
	v_exp_f32_e32 v127, v127
	v_med3_f32 v121, v121, s61, v172
	v_mul_f32_e32 v120, v120, v126
	v_add_f32_e32 v121, 1.0, v121
	v_mul_f32_e32 v120, v121, v120
	v_add_f32_e32 v121, 1.0, v127
	v_rcp_f32_e32 v121, v121
	v_mov_b32_e32 v126, v145
	v_cvt_pk_fp8_f32 v126, v124, v125
	v_med3_f32 v123, v123, s61, v172
	v_mul_f32_e32 v121, v122, v121
	v_add_f32_e32 v122, 1.0, v123
	v_pk_fma_f32 v[116:117], v[116:117], s[20:21], v[132:133] op_sel_hi:[1,0,1]
	v_mul_f32_e32 v121, v122, v121
	v_min_f32_e32 v116, 0x40e00000, v116
	v_cvt_pk_fp8_f32 v126, v120, v121 op_sel:[0,0,1]
	v_mul_f32_e32 v120, 0x3fd9db23, v116
	v_mul_f32_e32 v120, 0xbfb8aa3b, v120
	v_exp_f32_e32 v122, v120
	v_pk_fma_f32 v[118:119], v[118:119], s[20:21], v[134:135] op_sel_hi:[1,0,1]
	v_pk_fma_f32 v[112:113], v[112:113], s[20:21], v[128:129] op_sel_hi:[1,0,1]
	v_min_f32_e32 v118, 0x40e00000, v118
	v_add_f32_e32 v122, 1.0, v122
	v_mul_f32_e32 v123, 0x3fd9db23, v118
	v_rcp_f32_e32 v122, v122
	v_mul_f32_e32 v123, 0xbfb8aa3b, v123
	v_exp_f32_e32 v123, v123
	v_med3_f32 v117, v117, s61, v172
	v_mul_f32_e32 v116, v116, v122
	v_add_f32_e32 v117, 1.0, v117
	v_min_f32_e32 v112, 0x40e00000, v112
	v_add_f32_e32 v122, 1.0, v123
	v_mul_f32_e32 v116, v117, v116
	v_med3_f32 v117, v119, s61, v172
	v_mul_f32_e32 v119, 0x3fd9db23, v112
	v_rcp_f32_e32 v122, v122
	v_mul_f32_e32 v119, 0xbfb8aa3b, v119
	v_exp_f32_e32 v119, v119
	v_pk_fma_f32 v[114:115], v[114:115], s[20:21], v[130:131] op_sel_hi:[1,0,1]
	v_mul_f32_e32 v118, v118, v122
	v_add_f32_e32 v117, 1.0, v117
	v_min_f32_e32 v114, 0x40e00000, v114
	v_mul_f32_e32 v117, v117, v118
	v_add_f32_e32 v118, 1.0, v119
	v_mul_f32_e32 v119, 0x3fd9db23, v114
	v_rcp_f32_e32 v118, v118
	v_mul_f32_e32 v119, 0xbfb8aa3b, v119
	v_exp_f32_e32 v119, v119
	v_med3_f32 v113, v113, s61, v172
	v_mul_f32_e32 v112, v112, v118
	v_add_f32_e32 v113, 1.0, v113
	v_mul_f32_e32 v112, v113, v112
	v_add_f32_e32 v113, 1.0, v119
	v_rcp_f32_e32 v113, v113
	v_mov_b32_e32 v118, v145
	v_cvt_pk_fp8_f32 v118, v116, v117
	v_med3_f32 v115, v115, s61, v172
	v_mul_f32_e32 v113, v114, v113
	v_add_f32_e32 v114, 1.0, v115
	v_mul_f32_e32 v113, v114, v113
	v_cvt_pk_fp8_f32 v118, v112, v113 op_sel:[0,0,1]
	v_lshl_add_u64 v[176:177], s[16:17], 0, v[176:177]
	v_ashrrev_i32_e32 v149, 31, v148
	v_lshl_add_u64 v[120:121], v[176:177], 0, v[150:151]
	v_lshl_add_u64 v[112:113], v[176:177], 0, v[148:149]
	global_store_dword v[120:121], v126, off
	global_store_dword v[112:113], v118, off
.LBB0_1162:
	s_or_b64 exec, exec, s[10:11]
	v_add_u32_e32 v112, s39, v162
	v_cmp_gt_i32_e32 vcc, s38, v162
	s_nop 1
	v_cndmask_b32_e32 v144, -1, v112, vcc
	v_cmp_lt_i32_e32 vcc, -1, v144
	s_and_saveexec_b64 s[10:11], vcc
	s_cbranch_execz .LBB0_1164
	v_pk_fma_f32 v[108:109], v[108:109], s[20:21], v[140:141] op_sel_hi:[1,0,1]
	v_pk_fma_f32 v[110:111], v[110:111], s[20:21], v[142:143] op_sel_hi:[1,0,1]
	v_min_f32_e32 v108, 0x40e00000, v108
	v_mul_f32_e32 v114, 0x3fd9db23, v108
	v_mul_f32_e32 v114, 0xbfb8aa3b, v114
	v_exp_f32_e32 v114, v114
	v_min_f32_e32 v110, 0x40e00000, v110
	v_mul_f32_e32 v115, 0x3fd9db23, v110
	v_mul_f32_e32 v115, 0xbfb8aa3b, v115
	v_add_f32_e32 v114, 1.0, v114
	v_rcp_f32_e32 v114, v114
	v_exp_f32_e32 v115, v115
	v_pk_fma_f32 v[104:105], v[104:105], s[20:21], v[136:137] op_sel_hi:[1,0,1]
	v_med3_f32 v109, v109, s61, v172
	v_mul_f32_e32 v108, v108, v114
	v_add_f32_e32 v109, 1.0, v109
	v_min_f32_e32 v104, 0x40e00000, v104
	v_add_f32_e32 v114, 1.0, v115
	v_mul_f32_e32 v108, v109, v108
	v_med3_f32 v109, v111, s61, v172
	v_mul_f32_e32 v111, 0x3fd9db23, v104
	v_rcp_f32_e32 v114, v114
	v_mul_f32_e32 v111, 0xbfb8aa3b, v111
	v_exp_f32_e32 v111, v111
	v_pk_fma_f32 v[106:107], v[106:107], s[20:21], v[138:139] op_sel_hi:[1,0,1]
	v_mul_f32_e32 v110, v110, v114
	v_add_f32_e32 v109, 1.0, v109
	v_min_f32_e32 v106, 0x40e00000, v106
	v_mul_f32_e32 v109, v109, v110
	v_add_f32_e32 v110, 1.0, v111
	v_mul_f32_e32 v111, 0x3fd9db23, v106
	v_rcp_f32_e32 v110, v110
	v_mul_f32_e32 v111, 0xbfb8aa3b, v111
	v_exp_f32_e32 v111, v111
	v_med3_f32 v105, v105, s61, v172
	v_mul_f32_e32 v104, v104, v110
	v_add_f32_e32 v105, 1.0, v105
	v_mul_f32_e32 v104, v105, v104
	v_add_f32_e32 v105, 1.0, v111
	v_rcp_f32_e32 v105, v105
	v_mov_b32_e32 v110, v145
	v_cvt_pk_fp8_f32 v110, v108, v109
	v_med3_f32 v107, v107, s61, v172
	v_mul_f32_e32 v105, v106, v105
	v_add_f32_e32 v106, 1.0, v107
	v_pk_fma_f32 v[100:101], v[100:101], s[20:21], v[132:133] op_sel_hi:[1,0,1]
	v_mul_f32_e32 v105, v106, v105
	v_min_f32_e32 v100, 0x40e00000, v100
	v_cvt_pk_fp8_f32 v110, v104, v105 op_sel:[0,0,1]
	v_mul_f32_e32 v104, 0x3fd9db23, v100
	v_mul_f32_e32 v104, 0xbfb8aa3b, v104
	v_exp_f32_e32 v106, v104
	v_pk_fma_f32 v[102:103], v[102:103], s[20:21], v[134:135] op_sel_hi:[1,0,1]
	v_pk_fma_f32 v[96:97], v[96:97], s[20:21], v[128:129] op_sel_hi:[1,0,1]
	v_min_f32_e32 v102, 0x40e00000, v102
	v_add_f32_e32 v106, 1.0, v106
	v_mul_f32_e32 v107, 0x3fd9db23, v102
	v_rcp_f32_e32 v106, v106
	v_mul_f32_e32 v107, 0xbfb8aa3b, v107
	v_exp_f32_e32 v107, v107
	v_med3_f32 v101, v101, s61, v172
	v_mul_f32_e32 v100, v100, v106
	v_add_f32_e32 v101, 1.0, v101
	v_min_f32_e32 v96, 0x40e00000, v96
	v_add_f32_e32 v106, 1.0, v107
	v_mul_f32_e32 v100, v101, v100
	v_med3_f32 v101, v103, s61, v172
	v_mul_f32_e32 v103, 0x3fd9db23, v96
	v_rcp_f32_e32 v106, v106
	v_mul_f32_e32 v103, 0xbfb8aa3b, v103
	v_exp_f32_e32 v103, v103
	v_pk_fma_f32 v[98:99], v[98:99], s[20:21], v[130:131] op_sel_hi:[1,0,1]
	v_mul_f32_e32 v102, v102, v106
	v_add_f32_e32 v101, 1.0, v101
	v_min_f32_e32 v98, 0x40e00000, v98
	v_mul_f32_e32 v101, v101, v102
	v_add_f32_e32 v102, 1.0, v103
	v_mul_f32_e32 v103, 0x3fd9db23, v98
	v_rcp_f32_e32 v102, v102
	v_mul_f32_e32 v103, 0xbfb8aa3b, v103
	v_exp_f32_e32 v103, v103
	v_med3_f32 v97, v97, s61, v172
	v_mul_f32_e32 v96, v96, v102
	v_add_f32_e32 v97, 1.0, v97
	v_mul_f32_e32 v96, v97, v96
	v_add_f32_e32 v97, 1.0, v103
	v_rcp_f32_e32 v97, v97
	v_mov_b32_e32 v102, v145
	v_cvt_pk_fp8_f32 v102, v100, v101
	v_med3_f32 v99, v99, s61, v172
	v_mul_f32_e32 v97, v98, v97
	v_add_f32_e32 v98, 1.0, v99
	v_mul_f32_e32 v97, v98, v97
	v_cvt_pk_fp8_f32 v102, v96, v97 op_sel:[0,0,1]
	v_lshlrev_b64 v[112:113], 11, v[144:145]
	v_lshl_add_u64 v[112:113], s[16:17], 0, v[112:113]
	v_ashrrev_i32_e32 v149, 31, v148
	v_lshl_add_u64 v[104:105], v[112:113], 0, v[150:151]
	v_lshl_add_u64 v[96:97], v[112:113], 0, v[148:149]
	global_store_dword v[104:105], v110, off
	global_store_dword v[96:97], v102, off
.LBB0_1164:
	s_or_b64 exec, exec, s[10:11]
	v_add_u32_e32 v96, s39, v163
	v_cmp_gt_i32_e32 vcc, s38, v163
	s_nop 1
	v_cndmask_b32_e32 v144, -1, v96, vcc
	v_cmp_lt_i32_e32 vcc, -1, v144
	s_and_saveexec_b64 s[10:11], vcc
	s_cbranch_execz .LBB0_1166
	v_pk_fma_f32 v[92:93], v[92:93], s[20:21], v[140:141] op_sel_hi:[1,0,1]
	v_pk_fma_f32 v[94:95], v[94:95], s[20:21], v[142:143] op_sel_hi:[1,0,1]
	v_min_f32_e32 v92, 0x40e00000, v92
	v_mul_f32_e32 v98, 0x3fd9db23, v92
	v_mul_f32_e32 v98, 0xbfb8aa3b, v98
	v_exp_f32_e32 v98, v98
	v_min_f32_e32 v94, 0x40e00000, v94
	v_mul_f32_e32 v99, 0x3fd9db23, v94
	v_mul_f32_e32 v99, 0xbfb8aa3b, v99
	v_add_f32_e32 v98, 1.0, v98
	v_rcp_f32_e32 v98, v98
	v_exp_f32_e32 v99, v99
	v_pk_fma_f32 v[88:89], v[88:89], s[20:21], v[136:137] op_sel_hi:[1,0,1]
	v_med3_f32 v93, v93, s61, v172
	v_mul_f32_e32 v92, v92, v98
	v_add_f32_e32 v93, 1.0, v93
	v_min_f32_e32 v88, 0x40e00000, v88
	v_add_f32_e32 v98, 1.0, v99
	v_mul_f32_e32 v92, v93, v92
	v_med3_f32 v93, v95, s61, v172
	v_mul_f32_e32 v95, 0x3fd9db23, v88
	v_rcp_f32_e32 v98, v98
	v_mul_f32_e32 v95, 0xbfb8aa3b, v95
	v_exp_f32_e32 v95, v95
	v_pk_fma_f32 v[90:91], v[90:91], s[20:21], v[138:139] op_sel_hi:[1,0,1]
	v_mul_f32_e32 v94, v94, v98
	v_add_f32_e32 v93, 1.0, v93
	v_min_f32_e32 v90, 0x40e00000, v90
	v_mul_f32_e32 v93, v93, v94
	v_add_f32_e32 v94, 1.0, v95
	v_mul_f32_e32 v95, 0x3fd9db23, v90
	v_rcp_f32_e32 v94, v94
	v_mul_f32_e32 v95, 0xbfb8aa3b, v95
	v_exp_f32_e32 v95, v95
	v_med3_f32 v89, v89, s61, v172
	v_mul_f32_e32 v88, v88, v94
	v_add_f32_e32 v89, 1.0, v89
	v_mul_f32_e32 v88, v89, v88
	v_add_f32_e32 v89, 1.0, v95
	v_rcp_f32_e32 v89, v89
	v_mov_b32_e32 v94, v145
	v_cvt_pk_fp8_f32 v94, v92, v93
	v_med3_f32 v91, v91, s61, v172
	v_mul_f32_e32 v89, v90, v89
	v_add_f32_e32 v90, 1.0, v91
	v_pk_fma_f32 v[84:85], v[84:85], s[20:21], v[132:133] op_sel_hi:[1,0,1]
	v_mul_f32_e32 v89, v90, v89
	v_min_f32_e32 v84, 0x40e00000, v84
	v_cvt_pk_fp8_f32 v94, v88, v89 op_sel:[0,0,1]
	v_mul_f32_e32 v88, 0x3fd9db23, v84
	v_mul_f32_e32 v88, 0xbfb8aa3b, v88
	v_exp_f32_e32 v90, v88
	v_pk_fma_f32 v[86:87], v[86:87], s[20:21], v[134:135] op_sel_hi:[1,0,1]
	v_pk_fma_f32 v[80:81], v[80:81], s[20:21], v[128:129] op_sel_hi:[1,0,1]
	v_min_f32_e32 v86, 0x40e00000, v86
	v_add_f32_e32 v90, 1.0, v90
	v_mul_f32_e32 v91, 0x3fd9db23, v86
	v_rcp_f32_e32 v90, v90
	v_mul_f32_e32 v91, 0xbfb8aa3b, v91
	v_exp_f32_e32 v91, v91
	v_med3_f32 v85, v85, s61, v172
	v_mul_f32_e32 v84, v84, v90
	v_add_f32_e32 v85, 1.0, v85
	v_min_f32_e32 v80, 0x40e00000, v80
	v_add_f32_e32 v90, 1.0, v91
	v_mul_f32_e32 v84, v85, v84
	v_med3_f32 v85, v87, s61, v172
	v_mul_f32_e32 v87, 0x3fd9db23, v80
	v_rcp_f32_e32 v90, v90
	v_mul_f32_e32 v87, 0xbfb8aa3b, v87
	v_exp_f32_e32 v87, v87
	v_pk_fma_f32 v[82:83], v[82:83], s[20:21], v[130:131] op_sel_hi:[1,0,1]
	v_mul_f32_e32 v86, v86, v90
	v_add_f32_e32 v85, 1.0, v85
	v_min_f32_e32 v82, 0x40e00000, v82
	v_mul_f32_e32 v85, v85, v86
	v_add_f32_e32 v86, 1.0, v87
	v_mul_f32_e32 v87, 0x3fd9db23, v82
	v_rcp_f32_e32 v86, v86
	v_mul_f32_e32 v87, 0xbfb8aa3b, v87
	v_exp_f32_e32 v87, v87
	v_med3_f32 v81, v81, s61, v172
	v_mul_f32_e32 v80, v80, v86
	v_add_f32_e32 v81, 1.0, v81
	v_mul_f32_e32 v80, v81, v80
	v_add_f32_e32 v81, 1.0, v87
	v_rcp_f32_e32 v81, v81
	v_mov_b32_e32 v86, v145
	v_cvt_pk_fp8_f32 v86, v84, v85
	v_med3_f32 v83, v83, s61, v172
	v_mul_f32_e32 v81, v82, v81
	v_add_f32_e32 v82, 1.0, v83
	v_mul_f32_e32 v81, v82, v81
	v_cvt_pk_fp8_f32 v86, v80, v81 op_sel:[0,0,1]
	v_lshlrev_b64 v[96:97], 11, v[144:145]
	v_lshl_add_u64 v[96:97], s[16:17], 0, v[96:97]
	v_ashrrev_i32_e32 v149, 31, v148
	v_lshl_add_u64 v[88:89], v[96:97], 0, v[150:151]
	v_lshl_add_u64 v[80:81], v[96:97], 0, v[148:149]
	global_store_dword v[88:89], v94, off
	global_store_dword v[80:81], v86, off
.LBB0_1166:
	s_or_b64 exec, exec, s[10:11]
	v_add_u32_e32 v80, s39, v164
	v_cmp_gt_i32_e32 vcc, s38, v164
	s_nop 1
	v_cndmask_b32_e32 v144, -1, v80, vcc
	v_cmp_lt_i32_e32 vcc, -1, v144
	s_and_saveexec_b64 s[10:11], vcc
	s_cbranch_execz .LBB0_1168
	v_pk_fma_f32 v[76:77], v[76:77], s[20:21], v[140:141] op_sel_hi:[1,0,1]
	v_pk_fma_f32 v[78:79], v[78:79], s[20:21], v[142:143] op_sel_hi:[1,0,1]
	v_min_f32_e32 v76, 0x40e00000, v76
	v_mul_f32_e32 v82, 0x3fd9db23, v76
	v_mul_f32_e32 v82, 0xbfb8aa3b, v82
	v_exp_f32_e32 v82, v82
	v_min_f32_e32 v78, 0x40e00000, v78
	v_mul_f32_e32 v83, 0x3fd9db23, v78
	v_mul_f32_e32 v83, 0xbfb8aa3b, v83
	v_add_f32_e32 v82, 1.0, v82
	v_rcp_f32_e32 v82, v82
	v_exp_f32_e32 v83, v83
	v_pk_fma_f32 v[72:73], v[72:73], s[20:21], v[136:137] op_sel_hi:[1,0,1]
	v_med3_f32 v77, v77, s61, v172
	v_mul_f32_e32 v76, v76, v82
	v_add_f32_e32 v77, 1.0, v77
	v_min_f32_e32 v72, 0x40e00000, v72
	v_add_f32_e32 v82, 1.0, v83
	v_mul_f32_e32 v76, v77, v76
	v_med3_f32 v77, v79, s61, v172
	v_mul_f32_e32 v79, 0x3fd9db23, v72
	v_rcp_f32_e32 v82, v82
	v_mul_f32_e32 v79, 0xbfb8aa3b, v79
	v_exp_f32_e32 v79, v79
	v_pk_fma_f32 v[74:75], v[74:75], s[20:21], v[138:139] op_sel_hi:[1,0,1]
	v_mul_f32_e32 v78, v78, v82
	v_add_f32_e32 v77, 1.0, v77
	v_min_f32_e32 v74, 0x40e00000, v74
	v_mul_f32_e32 v77, v77, v78
	v_add_f32_e32 v78, 1.0, v79
	v_mul_f32_e32 v79, 0x3fd9db23, v74
	v_rcp_f32_e32 v78, v78
	v_mul_f32_e32 v79, 0xbfb8aa3b, v79
	v_exp_f32_e32 v79, v79
	v_med3_f32 v73, v73, s61, v172
	v_mul_f32_e32 v72, v72, v78
	v_add_f32_e32 v73, 1.0, v73
	v_mul_f32_e32 v72, v73, v72
	v_add_f32_e32 v73, 1.0, v79
	v_rcp_f32_e32 v73, v73
	v_mov_b32_e32 v78, v145
	v_cvt_pk_fp8_f32 v78, v76, v77
	v_med3_f32 v75, v75, s61, v172
	v_mul_f32_e32 v73, v74, v73
	v_add_f32_e32 v74, 1.0, v75
	v_pk_fma_f32 v[68:69], v[68:69], s[20:21], v[132:133] op_sel_hi:[1,0,1]
	v_mul_f32_e32 v73, v74, v73
	v_min_f32_e32 v68, 0x40e00000, v68
	v_cvt_pk_fp8_f32 v78, v72, v73 op_sel:[0,0,1]
	v_mul_f32_e32 v72, 0x3fd9db23, v68
	v_mul_f32_e32 v72, 0xbfb8aa3b, v72
	v_exp_f32_e32 v74, v72
	v_pk_fma_f32 v[70:71], v[70:71], s[20:21], v[134:135] op_sel_hi:[1,0,1]
	v_pk_fma_f32 v[64:65], v[64:65], s[20:21], v[128:129] op_sel_hi:[1,0,1]
	v_min_f32_e32 v70, 0x40e00000, v70
	v_add_f32_e32 v74, 1.0, v74
	v_mul_f32_e32 v75, 0x3fd9db23, v70
	v_rcp_f32_e32 v74, v74
	v_mul_f32_e32 v75, 0xbfb8aa3b, v75
	v_exp_f32_e32 v75, v75
	v_med3_f32 v69, v69, s61, v172
	v_mul_f32_e32 v68, v68, v74
	v_add_f32_e32 v69, 1.0, v69
	v_min_f32_e32 v64, 0x40e00000, v64
	v_add_f32_e32 v74, 1.0, v75
	v_mul_f32_e32 v68, v69, v68
	v_med3_f32 v69, v71, s61, v172
	v_mul_f32_e32 v71, 0x3fd9db23, v64
	v_rcp_f32_e32 v74, v74
	v_mul_f32_e32 v71, 0xbfb8aa3b, v71
	v_exp_f32_e32 v71, v71
	v_pk_fma_f32 v[66:67], v[66:67], s[20:21], v[130:131] op_sel_hi:[1,0,1]
	v_mul_f32_e32 v70, v70, v74
	v_add_f32_e32 v69, 1.0, v69
	v_min_f32_e32 v66, 0x40e00000, v66
	v_mul_f32_e32 v69, v69, v70
	v_add_f32_e32 v70, 1.0, v71
	v_mul_f32_e32 v71, 0x3fd9db23, v66
	v_rcp_f32_e32 v70, v70
	v_mul_f32_e32 v71, 0xbfb8aa3b, v71
	v_exp_f32_e32 v71, v71
	v_med3_f32 v65, v65, s61, v172
	v_mul_f32_e32 v64, v64, v70
	v_add_f32_e32 v65, 1.0, v65
	v_mul_f32_e32 v64, v65, v64
	v_add_f32_e32 v65, 1.0, v71
	v_rcp_f32_e32 v65, v65
	v_mov_b32_e32 v70, v145
	v_cvt_pk_fp8_f32 v70, v68, v69
	v_med3_f32 v67, v67, s61, v172
	v_mul_f32_e32 v65, v66, v65
	v_add_f32_e32 v66, 1.0, v67
	v_mul_f32_e32 v65, v66, v65
	v_cvt_pk_fp8_f32 v70, v64, v65 op_sel:[0,0,1]
	v_lshlrev_b64 v[80:81], 11, v[144:145]
	v_lshl_add_u64 v[80:81], s[16:17], 0, v[80:81]
	v_ashrrev_i32_e32 v149, 31, v148
	v_lshl_add_u64 v[72:73], v[80:81], 0, v[150:151]
	v_lshl_add_u64 v[64:65], v[80:81], 0, v[148:149]
	global_store_dword v[72:73], v78, off
	global_store_dword v[64:65], v70, off
.LBB0_1168:
	s_or_b64 exec, exec, s[10:11]
	v_add_u32_e32 v64, s39, v165
	v_cmp_gt_i32_e32 vcc, s38, v165
	s_nop 1
	v_cndmask_b32_e32 v144, -1, v64, vcc
	v_cmp_lt_i32_e32 vcc, -1, v144
	s_and_saveexec_b64 s[10:11], vcc
	s_cbranch_execz .LBB0_1170
	v_pk_fma_f32 v[60:61], v[60:61], s[20:21], v[140:141] op_sel_hi:[1,0,1]
	v_pk_fma_f32 v[62:63], v[62:63], s[20:21], v[142:143] op_sel_hi:[1,0,1]
	v_min_f32_e32 v60, 0x40e00000, v60
	v_mul_f32_e32 v66, 0x3fd9db23, v60
	v_mul_f32_e32 v66, 0xbfb8aa3b, v66
	v_exp_f32_e32 v66, v66
	v_min_f32_e32 v62, 0x40e00000, v62
	v_mul_f32_e32 v67, 0x3fd9db23, v62
	v_mul_f32_e32 v67, 0xbfb8aa3b, v67
	v_add_f32_e32 v66, 1.0, v66
	v_rcp_f32_e32 v66, v66
	v_exp_f32_e32 v67, v67
	v_pk_fma_f32 v[56:57], v[56:57], s[20:21], v[136:137] op_sel_hi:[1,0,1]
	v_med3_f32 v61, v61, s61, v172
	v_mul_f32_e32 v60, v60, v66
	v_add_f32_e32 v61, 1.0, v61
	v_min_f32_e32 v56, 0x40e00000, v56
	v_add_f32_e32 v66, 1.0, v67
	v_mul_f32_e32 v60, v61, v60
	v_med3_f32 v61, v63, s61, v172
	v_mul_f32_e32 v63, 0x3fd9db23, v56
	v_rcp_f32_e32 v66, v66
	v_mul_f32_e32 v63, 0xbfb8aa3b, v63
	v_exp_f32_e32 v63, v63
	v_pk_fma_f32 v[58:59], v[58:59], s[20:21], v[138:139] op_sel_hi:[1,0,1]
	v_mul_f32_e32 v62, v62, v66
	v_add_f32_e32 v61, 1.0, v61
	v_min_f32_e32 v58, 0x40e00000, v58
	v_mul_f32_e32 v61, v61, v62
	v_add_f32_e32 v62, 1.0, v63
	v_mul_f32_e32 v63, 0x3fd9db23, v58
	v_rcp_f32_e32 v62, v62
	v_mul_f32_e32 v63, 0xbfb8aa3b, v63
	v_exp_f32_e32 v63, v63
	v_med3_f32 v57, v57, s61, v172
	v_mul_f32_e32 v56, v56, v62
	v_add_f32_e32 v57, 1.0, v57
	v_mul_f32_e32 v56, v57, v56
	v_add_f32_e32 v57, 1.0, v63
	v_rcp_f32_e32 v57, v57
	v_mov_b32_e32 v62, v145
	v_cvt_pk_fp8_f32 v62, v60, v61
	v_med3_f32 v59, v59, s61, v172
	v_mul_f32_e32 v57, v58, v57
	v_add_f32_e32 v58, 1.0, v59
	v_pk_fma_f32 v[52:53], v[52:53], s[20:21], v[132:133] op_sel_hi:[1,0,1]
	v_mul_f32_e32 v57, v58, v57
	v_min_f32_e32 v52, 0x40e00000, v52
	v_cvt_pk_fp8_f32 v62, v56, v57 op_sel:[0,0,1]
	v_mul_f32_e32 v56, 0x3fd9db23, v52
	v_mul_f32_e32 v56, 0xbfb8aa3b, v56
	v_exp_f32_e32 v58, v56
	v_pk_fma_f32 v[54:55], v[54:55], s[20:21], v[134:135] op_sel_hi:[1,0,1]
	v_pk_fma_f32 v[48:49], v[48:49], s[20:21], v[128:129] op_sel_hi:[1,0,1]
	v_min_f32_e32 v54, 0x40e00000, v54
	v_add_f32_e32 v58, 1.0, v58
	v_mul_f32_e32 v59, 0x3fd9db23, v54
	v_rcp_f32_e32 v58, v58
	v_mul_f32_e32 v59, 0xbfb8aa3b, v59
	v_exp_f32_e32 v59, v59
	v_med3_f32 v53, v53, s61, v172
	v_mul_f32_e32 v52, v52, v58
	v_add_f32_e32 v53, 1.0, v53
	v_min_f32_e32 v48, 0x40e00000, v48
	v_add_f32_e32 v58, 1.0, v59
	v_mul_f32_e32 v52, v53, v52
	v_med3_f32 v53, v55, s61, v172
	v_mul_f32_e32 v55, 0x3fd9db23, v48
	v_rcp_f32_e32 v58, v58
	v_mul_f32_e32 v55, 0xbfb8aa3b, v55
	v_exp_f32_e32 v55, v55
	v_pk_fma_f32 v[50:51], v[50:51], s[20:21], v[130:131] op_sel_hi:[1,0,1]
	v_mul_f32_e32 v54, v54, v58
	v_add_f32_e32 v53, 1.0, v53
	v_min_f32_e32 v50, 0x40e00000, v50
	v_mul_f32_e32 v53, v53, v54
	v_add_f32_e32 v54, 1.0, v55
	v_mul_f32_e32 v55, 0x3fd9db23, v50
	v_rcp_f32_e32 v54, v54
	v_mul_f32_e32 v55, 0xbfb8aa3b, v55
	v_exp_f32_e32 v55, v55
	v_med3_f32 v49, v49, s61, v172
	v_mul_f32_e32 v48, v48, v54
	v_add_f32_e32 v49, 1.0, v49
	v_mul_f32_e32 v48, v49, v48
	v_add_f32_e32 v49, 1.0, v55
	v_rcp_f32_e32 v49, v49
	v_mov_b32_e32 v54, v145
	v_cvt_pk_fp8_f32 v54, v52, v53
	v_med3_f32 v51, v51, s61, v172
	v_mul_f32_e32 v49, v50, v49
	v_add_f32_e32 v50, 1.0, v51
	v_mul_f32_e32 v49, v50, v49
	v_cvt_pk_fp8_f32 v54, v48, v49 op_sel:[0,0,1]
	v_lshlrev_b64 v[64:65], 11, v[144:145]
	v_lshl_add_u64 v[64:65], s[16:17], 0, v[64:65]
	v_ashrrev_i32_e32 v149, 31, v148
	v_lshl_add_u64 v[56:57], v[64:65], 0, v[150:151]
	v_lshl_add_u64 v[48:49], v[64:65], 0, v[148:149]
	global_store_dword v[56:57], v62, off
	global_store_dword v[48:49], v54, off
.LBB0_1170:
	s_or_b64 exec, exec, s[10:11]
	v_add_u32_e32 v48, s39, v166
	v_cmp_gt_i32_e32 vcc, s38, v166
	s_nop 1
	v_cndmask_b32_e32 v144, -1, v48, vcc
	v_cmp_lt_i32_e32 vcc, -1, v144
	s_and_saveexec_b64 s[10:11], vcc
	s_cbranch_execz .LBB0_1172
	v_pk_fma_f32 v[44:45], v[44:45], s[20:21], v[140:141] op_sel_hi:[1,0,1]
	v_pk_fma_f32 v[46:47], v[46:47], s[20:21], v[142:143] op_sel_hi:[1,0,1]
	v_min_f32_e32 v44, 0x40e00000, v44
	v_mul_f32_e32 v50, 0x3fd9db23, v44
	v_mul_f32_e32 v50, 0xbfb8aa3b, v50
	v_exp_f32_e32 v50, v50
	v_min_f32_e32 v46, 0x40e00000, v46
	v_mul_f32_e32 v51, 0x3fd9db23, v46
	v_mul_f32_e32 v51, 0xbfb8aa3b, v51
	v_add_f32_e32 v50, 1.0, v50
	v_rcp_f32_e32 v50, v50
	v_exp_f32_e32 v51, v51
	v_pk_fma_f32 v[40:41], v[40:41], s[20:21], v[136:137] op_sel_hi:[1,0,1]
	v_med3_f32 v45, v45, s61, v172
	v_mul_f32_e32 v44, v44, v50
	v_add_f32_e32 v45, 1.0, v45
	v_min_f32_e32 v40, 0x40e00000, v40
	v_add_f32_e32 v50, 1.0, v51
	v_mul_f32_e32 v44, v45, v44
	v_med3_f32 v45, v47, s61, v172
	v_mul_f32_e32 v47, 0x3fd9db23, v40
	v_rcp_f32_e32 v50, v50
	v_mul_f32_e32 v47, 0xbfb8aa3b, v47
	v_exp_f32_e32 v47, v47
	v_pk_fma_f32 v[42:43], v[42:43], s[20:21], v[138:139] op_sel_hi:[1,0,1]
	v_mul_f32_e32 v46, v46, v50
	v_add_f32_e32 v45, 1.0, v45
	v_min_f32_e32 v42, 0x40e00000, v42
	v_mul_f32_e32 v45, v45, v46
	v_add_f32_e32 v46, 1.0, v47
	v_mul_f32_e32 v47, 0x3fd9db23, v42
	v_rcp_f32_e32 v46, v46
	v_mul_f32_e32 v47, 0xbfb8aa3b, v47
	v_exp_f32_e32 v47, v47
	v_med3_f32 v41, v41, s61, v172
	v_mul_f32_e32 v40, v40, v46
	v_add_f32_e32 v41, 1.0, v41
	v_mul_f32_e32 v40, v41, v40
	v_add_f32_e32 v41, 1.0, v47
	v_rcp_f32_e32 v41, v41
	v_mov_b32_e32 v46, v145
	v_cvt_pk_fp8_f32 v46, v44, v45
	v_med3_f32 v43, v43, s61, v172
	v_mul_f32_e32 v41, v42, v41
	v_add_f32_e32 v42, 1.0, v43
	v_pk_fma_f32 v[36:37], v[36:37], s[20:21], v[132:133] op_sel_hi:[1,0,1]
	v_mul_f32_e32 v41, v42, v41
	v_min_f32_e32 v36, 0x40e00000, v36
	v_cvt_pk_fp8_f32 v46, v40, v41 op_sel:[0,0,1]
	v_mul_f32_e32 v40, 0x3fd9db23, v36
	v_mul_f32_e32 v40, 0xbfb8aa3b, v40
	v_exp_f32_e32 v42, v40
	v_pk_fma_f32 v[38:39], v[38:39], s[20:21], v[134:135] op_sel_hi:[1,0,1]
	v_pk_fma_f32 v[32:33], v[32:33], s[20:21], v[128:129] op_sel_hi:[1,0,1]
	v_min_f32_e32 v38, 0x40e00000, v38
	v_add_f32_e32 v42, 1.0, v42
	v_mul_f32_e32 v43, 0x3fd9db23, v38
	v_rcp_f32_e32 v42, v42
	v_mul_f32_e32 v43, 0xbfb8aa3b, v43
	v_exp_f32_e32 v43, v43
	v_med3_f32 v37, v37, s61, v172
	v_mul_f32_e32 v36, v36, v42
	v_add_f32_e32 v37, 1.0, v37
	v_min_f32_e32 v32, 0x40e00000, v32
	v_add_f32_e32 v42, 1.0, v43
	v_mul_f32_e32 v36, v37, v36
	v_med3_f32 v37, v39, s61, v172
	v_mul_f32_e32 v39, 0x3fd9db23, v32
	v_rcp_f32_e32 v42, v42
	v_mul_f32_e32 v39, 0xbfb8aa3b, v39
	v_exp_f32_e32 v39, v39
	v_pk_fma_f32 v[34:35], v[34:35], s[20:21], v[130:131] op_sel_hi:[1,0,1]
	v_mul_f32_e32 v38, v38, v42
	v_add_f32_e32 v37, 1.0, v37
	v_min_f32_e32 v34, 0x40e00000, v34
	v_mul_f32_e32 v37, v37, v38
	v_add_f32_e32 v38, 1.0, v39
	v_mul_f32_e32 v39, 0x3fd9db23, v34
	v_rcp_f32_e32 v38, v38
	v_mul_f32_e32 v39, 0xbfb8aa3b, v39
	v_exp_f32_e32 v39, v39
	v_med3_f32 v33, v33, s61, v172
	v_mul_f32_e32 v32, v32, v38
	v_add_f32_e32 v33, 1.0, v33
	v_mul_f32_e32 v32, v33, v32
	v_add_f32_e32 v33, 1.0, v39
	v_rcp_f32_e32 v33, v33
	v_mov_b32_e32 v38, v145
	v_cvt_pk_fp8_f32 v38, v36, v37
	v_med3_f32 v35, v35, s61, v172
	v_mul_f32_e32 v33, v34, v33
	v_add_f32_e32 v34, 1.0, v35
	v_mul_f32_e32 v33, v34, v33
	v_cvt_pk_fp8_f32 v38, v32, v33 op_sel:[0,0,1]
	v_lshlrev_b64 v[48:49], 11, v[144:145]
	v_lshl_add_u64 v[48:49], s[16:17], 0, v[48:49]
	v_ashrrev_i32_e32 v149, 31, v148
	v_lshl_add_u64 v[40:41], v[48:49], 0, v[150:151]
	v_lshl_add_u64 v[32:33], v[48:49], 0, v[148:149]
	global_store_dword v[40:41], v46, off
	global_store_dword v[32:33], v38, off
.LBB0_1172:
	s_or_b64 exec, exec, s[10:11]
	v_add_u32_e32 v32, s39, v167
	v_cmp_gt_i32_e32 vcc, s38, v167
	s_nop 1
	v_cndmask_b32_e32 v144, -1, v32, vcc
	v_cmp_lt_i32_e32 vcc, -1, v144
	s_and_saveexec_b64 s[10:11], vcc
	s_cbranch_execz .LBB0_1174
	v_pk_fma_f32 v[28:29], v[28:29], s[20:21], v[140:141] op_sel_hi:[1,0,1]
	v_pk_fma_f32 v[30:31], v[30:31], s[20:21], v[142:143] op_sel_hi:[1,0,1]
	v_min_f32_e32 v28, 0x40e00000, v28
	v_mul_f32_e32 v34, 0x3fd9db23, v28
	v_mul_f32_e32 v34, 0xbfb8aa3b, v34
	v_exp_f32_e32 v34, v34
	v_min_f32_e32 v30, 0x40e00000, v30
	v_mul_f32_e32 v35, 0x3fd9db23, v30
	v_mul_f32_e32 v35, 0xbfb8aa3b, v35
	v_add_f32_e32 v34, 1.0, v34
	v_rcp_f32_e32 v34, v34
	v_exp_f32_e32 v35, v35
	v_pk_fma_f32 v[24:25], v[24:25], s[20:21], v[136:137] op_sel_hi:[1,0,1]
	v_med3_f32 v29, v29, s61, v172
	v_mul_f32_e32 v28, v28, v34
	v_add_f32_e32 v29, 1.0, v29
	v_min_f32_e32 v24, 0x40e00000, v24
	v_add_f32_e32 v34, 1.0, v35
	v_mul_f32_e32 v28, v29, v28
	v_med3_f32 v29, v31, s61, v172
	v_mul_f32_e32 v31, 0x3fd9db23, v24
	v_rcp_f32_e32 v34, v34
	v_mul_f32_e32 v31, 0xbfb8aa3b, v31
	v_exp_f32_e32 v31, v31
	v_pk_fma_f32 v[26:27], v[26:27], s[20:21], v[138:139] op_sel_hi:[1,0,1]
	v_mul_f32_e32 v30, v30, v34
	v_add_f32_e32 v29, 1.0, v29
	v_min_f32_e32 v26, 0x40e00000, v26
	v_mul_f32_e32 v29, v29, v30
	v_add_f32_e32 v30, 1.0, v31
	v_mul_f32_e32 v31, 0x3fd9db23, v26
	v_rcp_f32_e32 v30, v30
	v_mul_f32_e32 v31, 0xbfb8aa3b, v31
	v_exp_f32_e32 v31, v31
	v_med3_f32 v25, v25, s61, v172
	v_mul_f32_e32 v24, v24, v30
	v_add_f32_e32 v25, 1.0, v25
	v_mul_f32_e32 v24, v25, v24
	v_add_f32_e32 v25, 1.0, v31
	v_rcp_f32_e32 v25, v25
	v_mov_b32_e32 v30, v145
	v_cvt_pk_fp8_f32 v30, v28, v29
	v_med3_f32 v27, v27, s61, v172
	v_mul_f32_e32 v25, v26, v25
	v_add_f32_e32 v26, 1.0, v27
	v_pk_fma_f32 v[20:21], v[20:21], s[20:21], v[132:133] op_sel_hi:[1,0,1]
	v_mul_f32_e32 v25, v26, v25
	v_min_f32_e32 v20, 0x40e00000, v20
	v_cvt_pk_fp8_f32 v30, v24, v25 op_sel:[0,0,1]
	v_mul_f32_e32 v24, 0x3fd9db23, v20
	v_mul_f32_e32 v24, 0xbfb8aa3b, v24
	v_exp_f32_e32 v26, v24
	v_pk_fma_f32 v[22:23], v[22:23], s[20:21], v[134:135] op_sel_hi:[1,0,1]
	v_pk_fma_f32 v[16:17], v[16:17], s[20:21], v[128:129] op_sel_hi:[1,0,1]
	v_min_f32_e32 v22, 0x40e00000, v22
	v_add_f32_e32 v26, 1.0, v26
	v_mul_f32_e32 v27, 0x3fd9db23, v22
	v_rcp_f32_e32 v26, v26
	v_mul_f32_e32 v27, 0xbfb8aa3b, v27
	v_exp_f32_e32 v27, v27
	v_med3_f32 v21, v21, s61, v172
	v_mul_f32_e32 v20, v20, v26
	v_add_f32_e32 v21, 1.0, v21
	v_min_f32_e32 v16, 0x40e00000, v16
	v_add_f32_e32 v26, 1.0, v27
	v_mul_f32_e32 v20, v21, v20
	v_med3_f32 v21, v23, s61, v172
	v_mul_f32_e32 v23, 0x3fd9db23, v16
	v_rcp_f32_e32 v26, v26
	v_mul_f32_e32 v23, 0xbfb8aa3b, v23
	v_exp_f32_e32 v23, v23
	v_pk_fma_f32 v[18:19], v[18:19], s[20:21], v[130:131] op_sel_hi:[1,0,1]
	v_mul_f32_e32 v22, v22, v26
	v_add_f32_e32 v21, 1.0, v21
	v_min_f32_e32 v18, 0x40e00000, v18
	v_mul_f32_e32 v21, v21, v22
	v_add_f32_e32 v22, 1.0, v23
	v_mul_f32_e32 v23, 0x3fd9db23, v18
	v_rcp_f32_e32 v22, v22
	v_mul_f32_e32 v23, 0xbfb8aa3b, v23
	v_exp_f32_e32 v23, v23
	v_med3_f32 v17, v17, s61, v172
	v_mul_f32_e32 v16, v16, v22
	v_add_f32_e32 v17, 1.0, v17
	v_mul_f32_e32 v16, v17, v16
	v_add_f32_e32 v17, 1.0, v23
	v_rcp_f32_e32 v17, v17
	v_mov_b32_e32 v22, v145
	v_cvt_pk_fp8_f32 v22, v20, v21
	v_med3_f32 v19, v19, s61, v172
	v_mul_f32_e32 v17, v18, v17
	v_add_f32_e32 v18, 1.0, v19
	v_mul_f32_e32 v17, v18, v17
	v_cvt_pk_fp8_f32 v22, v16, v17 op_sel:[0,0,1]
	v_lshlrev_b64 v[32:33], 11, v[144:145]
	v_lshl_add_u64 v[32:33], s[16:17], 0, v[32:33]
	v_ashrrev_i32_e32 v149, 31, v148
	v_lshl_add_u64 v[24:25], v[32:33], 0, v[150:151]
	v_lshl_add_u64 v[16:17], v[32:33], 0, v[148:149]
	global_store_dword v[24:25], v30, off
	global_store_dword v[16:17], v22, off
.LBB0_1174:
	s_or_b64 exec, exec, s[10:11]
	v_add_u32_e32 v16, s39, v168
	v_cmp_gt_i32_e32 vcc, s38, v168
	s_nop 1
	v_cndmask_b32_e32 v144, -1, v16, vcc
	v_cmp_lt_i32_e32 vcc, -1, v144
	s_and_saveexec_b64 s[10:11], vcc
	s_cbranch_execz .LBB0_1176
	v_pk_fma_f32 v[12:13], v[12:13], s[20:21], v[140:141] op_sel_hi:[1,0,1]
	v_pk_fma_f32 v[14:15], v[14:15], s[20:21], v[142:143] op_sel_hi:[1,0,1]
	v_min_f32_e32 v12, 0x40e00000, v12
	v_mul_f32_e32 v18, 0x3fd9db23, v12
	v_mul_f32_e32 v18, 0xbfb8aa3b, v18
	v_exp_f32_e32 v18, v18
	v_min_f32_e32 v14, 0x40e00000, v14
	v_mul_f32_e32 v19, 0x3fd9db23, v14
	v_mul_f32_e32 v19, 0xbfb8aa3b, v19
	v_add_f32_e32 v18, 1.0, v18
	v_rcp_f32_e32 v18, v18
	v_exp_f32_e32 v19, v19
	v_pk_fma_f32 v[8:9], v[8:9], s[20:21], v[136:137] op_sel_hi:[1,0,1]
	v_med3_f32 v13, v13, s61, v172
	v_mul_f32_e32 v12, v12, v18
	v_add_f32_e32 v13, 1.0, v13
	v_min_f32_e32 v8, 0x40e00000, v8
	v_add_f32_e32 v18, 1.0, v19
	v_mul_f32_e32 v12, v13, v12
	v_med3_f32 v13, v15, s61, v172
	v_mul_f32_e32 v15, 0x3fd9db23, v8
	v_rcp_f32_e32 v18, v18
	v_mul_f32_e32 v15, 0xbfb8aa3b, v15
	v_exp_f32_e32 v15, v15
	v_pk_fma_f32 v[10:11], v[10:11], s[20:21], v[138:139] op_sel_hi:[1,0,1]
	v_mul_f32_e32 v14, v14, v18
	v_add_f32_e32 v13, 1.0, v13
	v_min_f32_e32 v10, 0x40e00000, v10
	v_mul_f32_e32 v13, v13, v14
	v_add_f32_e32 v14, 1.0, v15
	v_mul_f32_e32 v15, 0x3fd9db23, v10
	v_rcp_f32_e32 v14, v14
	v_mul_f32_e32 v15, 0xbfb8aa3b, v15
	v_exp_f32_e32 v15, v15
	v_med3_f32 v9, v9, s61, v172
	v_mul_f32_e32 v8, v8, v14
	v_add_f32_e32 v9, 1.0, v9
	v_mul_f32_e32 v8, v9, v8
	v_add_f32_e32 v9, 1.0, v15
	v_rcp_f32_e32 v9, v9
	v_mov_b32_e32 v14, v145
	v_cvt_pk_fp8_f32 v14, v12, v13
	v_med3_f32 v11, v11, s61, v172
	v_mul_f32_e32 v9, v10, v9
	v_add_f32_e32 v10, 1.0, v11
	v_pk_fma_f32 v[4:5], v[4:5], s[20:21], v[132:133] op_sel_hi:[1,0,1]
	v_mul_f32_e32 v9, v10, v9
	v_min_f32_e32 v4, 0x40e00000, v4
	v_cvt_pk_fp8_f32 v14, v8, v9 op_sel:[0,0,1]
	v_mul_f32_e32 v8, 0x3fd9db23, v4
	v_mul_f32_e32 v8, 0xbfb8aa3b, v8
	v_exp_f32_e32 v10, v8
	v_pk_fma_f32 v[6:7], v[6:7], s[20:21], v[134:135] op_sel_hi:[1,0,1]
	v_pk_fma_f32 v[0:1], v[0:1], s[20:21], v[128:129] op_sel_hi:[1,0,1]
	v_min_f32_e32 v6, 0x40e00000, v6
	v_add_f32_e32 v10, 1.0, v10
	v_mul_f32_e32 v11, 0x3fd9db23, v6
	v_rcp_f32_e32 v10, v10
	v_mul_f32_e32 v11, 0xbfb8aa3b, v11
	v_exp_f32_e32 v11, v11
	v_med3_f32 v5, v5, s61, v172
	v_mul_f32_e32 v4, v4, v10
	v_add_f32_e32 v5, 1.0, v5
	v_min_f32_e32 v0, 0x40e00000, v0
	v_add_f32_e32 v10, 1.0, v11
	v_mul_f32_e32 v4, v5, v4
	v_med3_f32 v5, v7, s61, v172
	v_mul_f32_e32 v7, 0x3fd9db23, v0
	v_rcp_f32_e32 v10, v10
	v_mul_f32_e32 v7, 0xbfb8aa3b, v7
	v_exp_f32_e32 v7, v7
	v_pk_fma_f32 v[2:3], v[2:3], s[20:21], v[130:131] op_sel_hi:[1,0,1]
	v_mul_f32_e32 v6, v6, v10
	v_add_f32_e32 v5, 1.0, v5
	v_min_f32_e32 v2, 0x40e00000, v2
	v_mul_f32_e32 v5, v5, v6
	v_add_f32_e32 v6, 1.0, v7
	v_mul_f32_e32 v7, 0x3fd9db23, v2
	v_rcp_f32_e32 v6, v6
	v_mul_f32_e32 v7, 0xbfb8aa3b, v7
	v_exp_f32_e32 v7, v7
	v_med3_f32 v1, v1, s61, v172
	v_mul_f32_e32 v0, v0, v6
	v_add_f32_e32 v1, 1.0, v1
	v_mul_f32_e32 v0, v1, v0
	v_add_f32_e32 v1, 1.0, v7
	v_rcp_f32_e32 v1, v1
	v_mov_b32_e32 v6, v145
	v_cvt_pk_fp8_f32 v6, v4, v5
	v_med3_f32 v3, v3, s61, v172
	v_mul_f32_e32 v1, v2, v1
	v_add_f32_e32 v2, 1.0, v3
	v_mul_f32_e32 v1, v2, v1
	v_cvt_pk_fp8_f32 v6, v0, v1 op_sel:[0,0,1]
	v_lshlrev_b64 v[16:17], 11, v[144:145]
	v_lshl_add_u64 v[16:17], s[16:17], 0, v[16:17]
	v_ashrrev_i32_e32 v149, 31, v148
	v_lshl_add_u64 v[8:9], v[16:17], 0, v[150:151]
	v_lshl_add_u64 v[0:1], v[16:17], 0, v[148:149]
	global_store_dword v[8:9], v14, off
	global_store_dword v[0:1], v6, off

.LBB0_1248:
	s_andn2_b64 vcc, exec, s[0:1]
	v_mov_b32_e32 v131, v185
	v_mov_b32_e32 v130, v184
	v_mov_b32_e32 v129, v183
	v_mov_b32_e32 v128, v182
	s_mov_b32 s81, s78
	s_mov_b32 s1, s76
	s_mov_b32 s0, s77
	v_mov_b32_e32 v146, v181
	s_mov_b32 s6, s80
	s_cbranch_vccz .LBB0_1276

.LBB0_1257:
	v_ashrrev_i32_e32 v147, 31, v146
	v_readlane_b32 s4, v253, 45
	v_lshlrev_b64 v[128:129], 13, v[146:147]
	v_readlane_b32 s16, v253, 57
	v_readlane_b32 s17, v253, 58
	v_readlane_b32 s14, v253, 55
	v_readlane_b32 s15, v253, 56
	v_lshl_add_u64 v[128:129], s[16:17], 0, v[128:129]
	v_cmp_gt_i32_e64 s[16:17], s81, v168
	v_readlane_b32 s12, v253, 53
	v_readlane_b32 s13, v253, 54
	v_cndmask_b32_e64 v144, 0, v168, s[16:17]
	v_cmp_gt_i32_e64 s[14:15], s81, v170
	v_readlane_b32 s10, v253, 51
	v_readlane_b32 s11, v253, 52
	v_lshlrev_b32_e32 v163, 2, v144
	v_cndmask_b32_e64 v144, 0, v170, s[14:15]
	v_cmp_gt_i32_e64 s[12:13], s81, v171
	v_readlane_b32 s8, v253, 49
	v_readlane_b32 s9, v253, 50
	v_lshlrev_b32_e32 v150, 2, v144
	v_cndmask_b32_e64 v144, 0, v171, s[12:13]
	v_cmp_gt_i32_e64 s[10:11], s81, v172
	v_lshl_or_b32 v148, s1, 8, v169
	s_ashr_i32 s1, s0, 31
	v_lshlrev_b64 v[164:165], 18, v[146:147]
	v_lshlrev_b32_e32 v152, 2, v144
	v_cndmask_b32_e64 v144, 0, v172, s[10:11]
	v_cmp_gt_i32_e64 s[8:9], s81, v173
	v_lshl_add_u64 v[146:147], s[34:35], 0, v[164:165]
	s_lshl_b64 s[0:1], s[0:1], 2
	v_lshlrev_b32_e32 v154, 2, v144
	v_cndmask_b32_e64 v144, 0, v173, s[8:9]
	v_readlane_b32 s5, v253, 46
	v_readlane_b32 s6, v253, 47
	v_readlane_b32 s7, v253, 48
	v_ashrrev_i32_e32 v149, 31, v148
	v_lshl_add_u64 v[146:147], v[146:147], 0, s[0:1]
	v_lshlrev_b64 v[192:193], 2, v[144:145]
	s_nop 15
	s_nop 15
	v_lshl_add_u64 v[132:133], v[148:149], 2, v[128:129]
	v_readfirstlane_b32 s4, v146
	v_readfirstlane_b32 s5, v147
	v_lshl_add_u64 v[186:187], v[146:147], 0, v[192:193]
	v_cmp_gt_i32_e64 s[6:7], s81, v174
	global_load_dwordx4 v[136:139], v[132:133], off offset:16
	global_load_dwordx4 v[140:143], v[132:133], off
	global_load_dwordx4 v[128:131], v[132:133], off offset:528
	s_nop 0
	global_load_dwordx4 v[132:135], v[132:133], off offset:512
	v_cndmask_b32_e64 v144, 0, v174, s[6:7]
	global_load_dword v162, v163, s[4:5]
	global_load_dword v191, v150, s[4:5]
	global_load_dword v190, v152, s[4:5]
	global_load_dword v188, v[186:187], off
	global_load_dword v189, v154, s[4:5]
	v_cmp_gt_i32_e64 s[4:5], s81, v175
	v_lshlrev_b64 v[194:195], 2, v[144:145]
	v_cmp_gt_i32_e32 vcc, s81, v176
	v_cndmask_b32_e64 v144, 0, v175, s[4:5]
	v_lshlrev_b64 v[196:197], 2, v[144:145]
	v_lshl_add_u64 v[186:187], v[146:147], 0, v[194:195]
	v_lshl_add_u64 v[198:199], v[146:147], 0, v[196:197]
	v_cndmask_b32_e32 v144, 0, v176, vcc
	v_lshl_add_u64 v[164:165], s[30:31], 0, v[164:165]
	global_load_dword v187, v[186:187], off
	v_lshl_add_u64 v[164:165], v[164:165], 0, s[0:1]
	global_load_dword v186, v[198:199], off
	v_lshlrev_b64 v[198:199], 2, v[144:145]
	v_lshl_add_u64 v[146:147], v[146:147], 0, v[198:199]
	v_readfirstlane_b32 s0, v164
	v_readfirstlane_b32 s1, v165
	v_lshl_add_u64 v[192:193], v[164:165], 0, v[192:193]
	global_load_dword v147, v[146:147], off
	s_nop 2
	global_load_dword v160, v150, s[0:1]
	global_load_dword v158, v152, s[0:1]
	global_load_dword v156, v154, s[0:1]
	v_readlane_b32 s18, v253, 59
	global_load_dword v154, v[192:193], off
	v_lshl_add_u64 v[192:193], v[164:165], 0, v[194:195]
	global_load_dword v152, v[192:193], off
	v_lshl_add_u64 v[192:193], v[164:165], 0, v[196:197]
	global_load_dword v150, v[192:193], off
	v_lshl_add_u64 v[192:193], v[164:165], 0, v[198:199]
	global_load_dword v146, v[192:193], off
	v_readlane_b32 s19, v253, 60
	s_waitcnt vmcnt(0)
	v_cndmask_b32_e64 v162, -1, v162, s[16:17]
	v_cmp_lt_i32_e64 s[0:1], -1, v162
	s_and_saveexec_b64 s[16:17], s[0:1]
	s_cbranch_execz .LBB0_1259
	v_readfirstlane_b32 s0, v164
	v_readfirstlane_b32 s1, v165
	v_pk_fma_f32 v[124:125], v[124:125], s[40:41], v[140:141] op_sel_hi:[1,0,1]
	v_pk_fma_f32 v[120:121], v[120:121], s[40:41], v[136:137] op_sel_hi:[1,0,1]
	v_pk_fma_f32 v[116:117], v[116:117], s[40:41], v[132:133] op_sel_hi:[1,0,1]
	v_pk_fma_f32 v[112:113], v[112:113], s[40:41], v[128:129] op_sel_hi:[1,0,1]
	v_mov_b32_e32 v164, v145
	global_load_dword v144, v163, s[0:1]
	v_mov_b32_e32 v165, v145
	v_pk_fma_f32 v[126:127], v[126:127], s[40:41], v[142:143] op_sel_hi:[1,0,1]
	v_pk_fma_f32 v[122:123], v[122:123], s[40:41], v[138:139] op_sel_hi:[1,0,1]
	v_mov_b32_e32 v192, v145
	v_mov_b32_e32 v193, v145
	v_pk_fma_f32 v[118:119], v[118:119], s[40:41], v[134:135] op_sel_hi:[1,0,1]
	v_pk_fma_f32 v[114:115], v[114:115], s[40:41], v[130:131] op_sel_hi:[1,0,1]
	v_mov_b32_e32 v163, v145
	v_lshlrev_b64 v[162:163], 11, v[162:163]
	s_waitcnt vmcnt(0)
	v_pk_mul_f32 v[124:125], v[124:125], v[144:145] op_sel_hi:[1,0]
	v_pk_mul_f32 v[120:121], v[120:121], v[144:145] op_sel_hi:[1,0]
	v_pk_mul_f32 v[116:117], v[116:117], v[144:145] op_sel_hi:[1,0]
	v_pk_mul_f32 v[112:113], v[112:113], v[144:145] op_sel_hi:[1,0]
	v_mul_f32_e32 v124, 0x41800000, v124
	v_mul_f32_e32 v125, 0x41800000, v125
	v_mul_f32_e32 v120, 0x41800000, v120
	v_mul_f32_e32 v121, 0x41800000, v121
	v_mul_f32_e32 v116, 0x41800000, v116
	v_mul_f32_e32 v117, 0x41800000, v117
	v_mul_f32_e32 v112, 0x41800000, v112
	v_mul_f32_e32 v113, 0x41800000, v113
	v_med3_f32 v124, v124, s75, v180
	v_med3_f32 v125, v125, s75, v180
	v_med3_f32 v120, v120, s75, v180
	v_med3_f32 v121, v121, s75, v180
	v_med3_f32 v116, v116, s75, v180
	v_med3_f32 v117, v117, s75, v180
	v_med3_f32 v112, v112, s75, v180
	v_med3_f32 v113, v113, s75, v180
	v_cvt_pk_fp8_f32 v164, v124, v125
	v_cvt_pk_fp8_f32 v165, v120, v121
	v_pk_mul_f32 v[126:127], v[126:127], v[144:145] op_sel_hi:[1,0]
	v_pk_mul_f32 v[122:123], v[122:123], v[144:145] op_sel_hi:[1,0]
	v_cvt_pk_fp8_f32 v192, v116, v117
	v_cvt_pk_fp8_f32 v193, v112, v113
	v_pk_mul_f32 v[118:119], v[118:119], v[144:145] op_sel_hi:[1,0]
	v_pk_mul_f32 v[114:115], v[114:115], v[144:145] op_sel_hi:[1,0]
	v_mul_f32_e32 v126, 0x41800000, v126
	v_mul_f32_e32 v127, 0x41800000, v127
	v_mul_f32_e32 v122, 0x41800000, v122
	v_mul_f32_e32 v123, 0x41800000, v123
	v_mul_f32_e32 v118, 0x41800000, v118
	v_mul_f32_e32 v119, 0x41800000, v119
	v_mul_f32_e32 v114, 0x41800000, v114
	v_mul_f32_e32 v115, 0x41800000, v115
	v_med3_f32 v126, v126, s75, v180
	v_med3_f32 v127, v127, s75, v180
	v_med3_f32 v122, v122, s75, v180
	v_med3_f32 v123, v123, s75, v180
	v_med3_f32 v118, v118, s75, v180
	v_med3_f32 v119, v119, s75, v180
	v_med3_f32 v114, v114, s75, v180
	v_med3_f32 v115, v115, s75, v180
	v_cvt_pk_fp8_f32 v164, v126, v127 op_sel:[0,0,1]
	v_cvt_pk_fp8_f32 v165, v122, v123 op_sel:[0,0,1]
	v_cvt_pk_fp8_f32 v192, v118, v119 op_sel:[0,0,1]
	v_cvt_pk_fp8_f32 v193, v114, v115 op_sel:[0,0,1]
	v_lshl_add_u64 v[112:113], s[36:37], 0, v[162:163]
	v_lshl_add_u64 v[112:113], v[112:113], 0, v[148:149]
	global_store_dwordx2 v[112:113], v[164:165], off
	global_store_dwordx2 v[112:113], v[192:193], off offset:128
.LBB0_1259:
	s_or_b64 exec, exec, s[16:17]
	v_cndmask_b32_e64 v144, -1, v191, s[14:15]
	v_cmp_lt_i32_e64 s[0:1], -1, v144
	s_and_saveexec_b64 s[14:15], s[0:1]
	s_cbranch_execz .LBB0_1261
	v_pk_fma_f32 v[108:109], v[108:109], s[40:41], v[140:141] op_sel_hi:[1,0,1]
	v_pk_fma_f32 v[110:111], v[110:111], s[40:41], v[142:143] op_sel_hi:[1,0,1]
	v_pk_mul_f32 v[108:109], v[108:109], v[160:161] op_sel_hi:[1,0]
	v_pk_mul_f32 v[110:111], v[110:111], v[160:161] op_sel_hi:[1,0]
	v_mul_f32_e32 v108, 0x41800000, v108
	v_mul_f32_e32 v109, 0x41800000, v109
	v_med3_f32 v114, v108, s75, v180
	v_med3_f32 v109, v109, s75, v180
	v_mov_b32_e32 v108, v145
	v_cvt_pk_fp8_f32 v108, v114, v109
	v_pk_fma_f32 v[104:105], v[104:105], s[40:41], v[136:137] op_sel_hi:[1,0,1]
	v_mul_f32_e32 v110, 0x41800000, v110
	v_pk_mul_f32 v[104:105], v[104:105], v[160:161] op_sel_hi:[1,0]
	v_mul_f32_e32 v109, 0x41800000, v111
	v_med3_f32 v110, v110, s75, v180
	v_med3_f32 v109, v109, s75, v180
	v_mul_f32_e32 v104, 0x41800000, v104
	v_mul_f32_e32 v105, 0x41800000, v105
	v_cvt_pk_fp8_f32 v108, v110, v109 op_sel:[0,0,1]
	v_med3_f32 v104, v104, s75, v180
	v_med3_f32 v105, v105, s75, v180
	v_mov_b32_e32 v109, v145
	v_pk_fma_f32 v[106:107], v[106:107], s[40:41], v[138:139] op_sel_hi:[1,0,1]
	v_cvt_pk_fp8_f32 v109, v104, v105
	v_pk_mul_f32 v[106:107], v[106:107], v[160:161] op_sel_hi:[1,0]
	v_pk_fma_f32 v[100:101], v[100:101], s[40:41], v[132:133] op_sel_hi:[1,0,1]
	v_mul_f32_e32 v106, 0x41800000, v106
	v_mul_f32_e32 v104, 0x41800000, v107
	v_pk_mul_f32 v[100:101], v[100:101], v[160:161] op_sel_hi:[1,0]
	v_med3_f32 v105, v106, s75, v180
	v_med3_f32 v104, v104, s75, v180
	v_mul_f32_e32 v100, 0x41800000, v100
	v_mul_f32_e32 v101, 0x41800000, v101
	v_cvt_pk_fp8_f32 v109, v105, v104 op_sel:[0,0,1]
	v_med3_f32 v104, v100, s75, v180
	v_med3_f32 v101, v101, s75, v180
	v_mov_b32_e32 v100, v145
	v_pk_fma_f32 v[102:103], v[102:103], s[40:41], v[134:135] op_sel_hi:[1,0,1]
	v_cvt_pk_fp8_f32 v100, v104, v101
	v_pk_mul_f32 v[102:103], v[102:103], v[160:161] op_sel_hi:[1,0]
	v_pk_fma_f32 v[96:97], v[96:97], s[40:41], v[128:129] op_sel_hi:[1,0,1]
	v_mul_f32_e32 v102, 0x41800000, v102
	v_pk_mul_f32 v[96:97], v[96:97], v[160:161] op_sel_hi:[1,0]
	v_mul_f32_e32 v101, 0x41800000, v103
	v_med3_f32 v102, v102, s75, v180
	v_med3_f32 v101, v101, s75, v180
	v_mul_f32_e32 v96, 0x41800000, v96
	v_mul_f32_e32 v97, 0x41800000, v97
	v_cvt_pk_fp8_f32 v100, v102, v101 op_sel:[0,0,1]
	v_med3_f32 v96, v96, s75, v180
	v_med3_f32 v97, v97, s75, v180
	v_mov_b32_e32 v101, v145
	v_pk_fma_f32 v[98:99], v[98:99], s[40:41], v[130:131] op_sel_hi:[1,0,1]
	v_cvt_pk_fp8_f32 v101, v96, v97
	v_pk_mul_f32 v[98:99], v[98:99], v[160:161] op_sel_hi:[1,0]
	v_lshlrev_b64 v[112:113], 11, v[144:145]
	v_mul_f32_e32 v98, 0x41800000, v98
	v_mul_f32_e32 v96, 0x41800000, v99
	v_med3_f32 v97, v98, s75, v180
	v_med3_f32 v96, v96, s75, v180
	v_cvt_pk_fp8_f32 v101, v97, v96 op_sel:[0,0,1]
	v_lshl_add_u64 v[96:97], s[36:37], 0, v[112:113]
	v_lshl_add_u64 v[96:97], v[96:97], 0, v[148:149]
	global_store_dwordx2 v[96:97], v[108:109], off
	global_store_dwordx2 v[96:97], v[100:101], off offset:128
.LBB0_1261:
	s_or_b64 exec, exec, s[14:15]
	v_cndmask_b32_e64 v144, -1, v190, s[12:13]
	v_cmp_lt_i32_e64 s[0:1], -1, v144
	s_and_saveexec_b64 s[12:13], s[0:1]
	s_cbranch_execz .LBB0_1263
	v_pk_fma_f32 v[92:93], v[92:93], s[40:41], v[140:141] op_sel_hi:[1,0,1]
	v_pk_fma_f32 v[94:95], v[94:95], s[40:41], v[142:143] op_sel_hi:[1,0,1]
	v_pk_mul_f32 v[92:93], v[92:93], v[158:159] op_sel_hi:[1,0]
	v_pk_mul_f32 v[94:95], v[94:95], v[158:159] op_sel_hi:[1,0]
	v_mul_f32_e32 v92, 0x41800000, v92
	v_mul_f32_e32 v93, 0x41800000, v93
	v_med3_f32 v98, v92, s75, v180
	v_med3_f32 v93, v93, s75, v180
	v_mov_b32_e32 v92, v145
	v_cvt_pk_fp8_f32 v92, v98, v93
	v_pk_fma_f32 v[88:89], v[88:89], s[40:41], v[136:137] op_sel_hi:[1,0,1]
	v_mul_f32_e32 v94, 0x41800000, v94
	v_pk_mul_f32 v[88:89], v[88:89], v[158:159] op_sel_hi:[1,0]
	v_mul_f32_e32 v93, 0x41800000, v95
	v_med3_f32 v94, v94, s75, v180
	v_med3_f32 v93, v93, s75, v180
	v_mul_f32_e32 v88, 0x41800000, v88
	v_mul_f32_e32 v89, 0x41800000, v89
	v_cvt_pk_fp8_f32 v92, v94, v93 op_sel:[0,0,1]
	v_med3_f32 v88, v88, s75, v180
	v_med3_f32 v89, v89, s75, v180
	v_mov_b32_e32 v93, v145
	v_pk_fma_f32 v[90:91], v[90:91], s[40:41], v[138:139] op_sel_hi:[1,0,1]
	v_cvt_pk_fp8_f32 v93, v88, v89
	v_pk_mul_f32 v[90:91], v[90:91], v[158:159] op_sel_hi:[1,0]
	v_pk_fma_f32 v[84:85], v[84:85], s[40:41], v[132:133] op_sel_hi:[1,0,1]
	v_mul_f32_e32 v90, 0x41800000, v90
	v_mul_f32_e32 v88, 0x41800000, v91
	v_pk_mul_f32 v[84:85], v[84:85], v[158:159] op_sel_hi:[1,0]
	v_med3_f32 v89, v90, s75, v180
	v_med3_f32 v88, v88, s75, v180
	v_mul_f32_e32 v84, 0x41800000, v84
	v_mul_f32_e32 v85, 0x41800000, v85
	v_cvt_pk_fp8_f32 v93, v89, v88 op_sel:[0,0,1]
	v_med3_f32 v88, v84, s75, v180
	v_med3_f32 v85, v85, s75, v180
	v_mov_b32_e32 v84, v145
	v_pk_fma_f32 v[86:87], v[86:87], s[40:41], v[134:135] op_sel_hi:[1,0,1]
	v_cvt_pk_fp8_f32 v84, v88, v85
	v_pk_mul_f32 v[86:87], v[86:87], v[158:159] op_sel_hi:[1,0]
	v_pk_fma_f32 v[80:81], v[80:81], s[40:41], v[128:129] op_sel_hi:[1,0,1]
	v_mul_f32_e32 v86, 0x41800000, v86
	v_pk_mul_f32 v[80:81], v[80:81], v[158:159] op_sel_hi:[1,0]
	v_mul_f32_e32 v85, 0x41800000, v87
	v_med3_f32 v86, v86, s75, v180
	v_med3_f32 v85, v85, s75, v180
	v_mul_f32_e32 v80, 0x41800000, v80
	v_mul_f32_e32 v81, 0x41800000, v81
	v_cvt_pk_fp8_f32 v84, v86, v85 op_sel:[0,0,1]
	v_med3_f32 v80, v80, s75, v180
	v_med3_f32 v81, v81, s75, v180
	v_mov_b32_e32 v85, v145
	v_pk_fma_f32 v[82:83], v[82:83], s[40:41], v[130:131] op_sel_hi:[1,0,1]
	v_cvt_pk_fp8_f32 v85, v80, v81
	v_pk_mul_f32 v[82:83], v[82:83], v[158:159] op_sel_hi:[1,0]
	v_lshlrev_b64 v[96:97], 11, v[144:145]
	v_mul_f32_e32 v82, 0x41800000, v82
	v_mul_f32_e32 v80, 0x41800000, v83
	v_med3_f32 v81, v82, s75, v180
	v_med3_f32 v80, v80, s75, v180
	v_cvt_pk_fp8_f32 v85, v81, v80 op_sel:[0,0,1]
	v_lshl_add_u64 v[80:81], s[36:37], 0, v[96:97]
	v_lshl_add_u64 v[80:81], v[80:81], 0, v[148:149]
	global_store_dwordx2 v[80:81], v[92:93], off
	global_store_dwordx2 v[80:81], v[84:85], off offset:128
.LBB0_1263:
	s_or_b64 exec, exec, s[12:13]
	v_cndmask_b32_e64 v144, -1, v189, s[10:11]
	v_cmp_lt_i32_e64 s[0:1], -1, v144
	s_and_saveexec_b64 s[10:11], s[0:1]
	s_cbranch_execz .LBB0_1265
	v_pk_fma_f32 v[76:77], v[76:77], s[40:41], v[140:141] op_sel_hi:[1,0,1]
	v_pk_fma_f32 v[78:79], v[78:79], s[40:41], v[142:143] op_sel_hi:[1,0,1]
	v_pk_mul_f32 v[76:77], v[76:77], v[156:157] op_sel_hi:[1,0]
	v_pk_mul_f32 v[78:79], v[78:79], v[156:157] op_sel_hi:[1,0]
	v_mul_f32_e32 v76, 0x41800000, v76
	v_mul_f32_e32 v77, 0x41800000, v77
	v_med3_f32 v82, v76, s75, v180
	v_med3_f32 v77, v77, s75, v180
	v_mov_b32_e32 v76, v145
	v_cvt_pk_fp8_f32 v76, v82, v77
	v_pk_fma_f32 v[72:73], v[72:73], s[40:41], v[136:137] op_sel_hi:[1,0,1]
	v_mul_f32_e32 v78, 0x41800000, v78
	v_pk_mul_f32 v[72:73], v[72:73], v[156:157] op_sel_hi:[1,0]
	v_mul_f32_e32 v77, 0x41800000, v79
	v_med3_f32 v78, v78, s75, v180
	v_med3_f32 v77, v77, s75, v180
	v_mul_f32_e32 v72, 0x41800000, v72
	v_mul_f32_e32 v73, 0x41800000, v73
	v_cvt_pk_fp8_f32 v76, v78, v77 op_sel:[0,0,1]
	v_med3_f32 v72, v72, s75, v180
	v_med3_f32 v73, v73, s75, v180
	v_mov_b32_e32 v77, v145
	v_pk_fma_f32 v[74:75], v[74:75], s[40:41], v[138:139] op_sel_hi:[1,0,1]
	v_cvt_pk_fp8_f32 v77, v72, v73
	v_pk_mul_f32 v[74:75], v[74:75], v[156:157] op_sel_hi:[1,0]
	v_pk_fma_f32 v[68:69], v[68:69], s[40:41], v[132:133] op_sel_hi:[1,0,1]
	v_mul_f32_e32 v74, 0x41800000, v74
	v_mul_f32_e32 v72, 0x41800000, v75
	v_pk_mul_f32 v[68:69], v[68:69], v[156:157] op_sel_hi:[1,0]
	v_med3_f32 v73, v74, s75, v180
	v_med3_f32 v72, v72, s75, v180
	v_mul_f32_e32 v68, 0x41800000, v68
	v_mul_f32_e32 v69, 0x41800000, v69
	v_cvt_pk_fp8_f32 v77, v73, v72 op_sel:[0,0,1]
	v_med3_f32 v72, v68, s75, v180
	v_med3_f32 v69, v69, s75, v180
	v_mov_b32_e32 v68, v145
	v_pk_fma_f32 v[70:71], v[70:71], s[40:41], v[134:135] op_sel_hi:[1,0,1]
	v_cvt_pk_fp8_f32 v68, v72, v69
	v_pk_mul_f32 v[70:71], v[70:71], v[156:157] op_sel_hi:[1,0]
	v_pk_fma_f32 v[64:65], v[64:65], s[40:41], v[128:129] op_sel_hi:[1,0,1]
	v_mul_f32_e32 v70, 0x41800000, v70
	v_pk_mul_f32 v[64:65], v[64:65], v[156:157] op_sel_hi:[1,0]
	v_mul_f32_e32 v69, 0x41800000, v71
	v_med3_f32 v70, v70, s75, v180
	v_med3_f32 v69, v69, s75, v180
	v_mul_f32_e32 v64, 0x41800000, v64
	v_mul_f32_e32 v65, 0x41800000, v65
	v_cvt_pk_fp8_f32 v68, v70, v69 op_sel:[0,0,1]
	v_med3_f32 v64, v64, s75, v180
	v_med3_f32 v65, v65, s75, v180
	v_mov_b32_e32 v69, v145
	v_pk_fma_f32 v[66:67], v[66:67], s[40:41], v[130:131] op_sel_hi:[1,0,1]
	v_cvt_pk_fp8_f32 v69, v64, v65
	v_pk_mul_f32 v[66:67], v[66:67], v[156:157] op_sel_hi:[1,0]
	v_lshlrev_b64 v[80:81], 11, v[144:145]
	v_mul_f32_e32 v66, 0x41800000, v66
	v_mul_f32_e32 v64, 0x41800000, v67
	v_med3_f32 v65, v66, s75, v180
	v_med3_f32 v64, v64, s75, v180
	v_cvt_pk_fp8_f32 v69, v65, v64 op_sel:[0,0,1]
	v_lshl_add_u64 v[64:65], s[36:37], 0, v[80:81]
	v_lshl_add_u64 v[64:65], v[64:65], 0, v[148:149]
	global_store_dwordx2 v[64:65], v[76:77], off
	global_store_dwordx2 v[64:65], v[68:69], off offset:128
.LBB0_1265:
	s_or_b64 exec, exec, s[10:11]
	v_cndmask_b32_e64 v144, -1, v188, s[8:9]
	v_cmp_lt_i32_e64 s[0:1], -1, v144
	s_and_saveexec_b64 s[8:9], s[0:1]
	s_cbranch_execz .LBB0_1267
	v_pk_fma_f32 v[60:61], v[60:61], s[40:41], v[140:141] op_sel_hi:[1,0,1]
	v_pk_fma_f32 v[62:63], v[62:63], s[40:41], v[142:143] op_sel_hi:[1,0,1]
	v_pk_mul_f32 v[60:61], v[60:61], v[154:155] op_sel_hi:[1,0]
	v_pk_mul_f32 v[62:63], v[62:63], v[154:155] op_sel_hi:[1,0]
	v_mul_f32_e32 v60, 0x41800000, v60
	v_mul_f32_e32 v61, 0x41800000, v61
	v_med3_f32 v66, v60, s75, v180
	v_med3_f32 v61, v61, s75, v180
	v_mov_b32_e32 v60, v145
	v_cvt_pk_fp8_f32 v60, v66, v61
	v_pk_fma_f32 v[56:57], v[56:57], s[40:41], v[136:137] op_sel_hi:[1,0,1]
	v_mul_f32_e32 v62, 0x41800000, v62
	v_pk_mul_f32 v[56:57], v[56:57], v[154:155] op_sel_hi:[1,0]
	v_mul_f32_e32 v61, 0x41800000, v63
	v_med3_f32 v62, v62, s75, v180
	v_med3_f32 v61, v61, s75, v180
	v_mul_f32_e32 v56, 0x41800000, v56
	v_mul_f32_e32 v57, 0x41800000, v57
	v_cvt_pk_fp8_f32 v60, v62, v61 op_sel:[0,0,1]
	v_med3_f32 v56, v56, s75, v180
	v_med3_f32 v57, v57, s75, v180
	v_mov_b32_e32 v61, v145
	v_pk_fma_f32 v[58:59], v[58:59], s[40:41], v[138:139] op_sel_hi:[1,0,1]
	v_cvt_pk_fp8_f32 v61, v56, v57
	v_pk_mul_f32 v[58:59], v[58:59], v[154:155] op_sel_hi:[1,0]
	v_pk_fma_f32 v[52:53], v[52:53], s[40:41], v[132:133] op_sel_hi:[1,0,1]
	v_mul_f32_e32 v58, 0x41800000, v58
	v_mul_f32_e32 v56, 0x41800000, v59
	v_pk_mul_f32 v[52:53], v[52:53], v[154:155] op_sel_hi:[1,0]
	v_med3_f32 v57, v58, s75, v180
	v_med3_f32 v56, v56, s75, v180
	v_mul_f32_e32 v52, 0x41800000, v52
	v_mul_f32_e32 v53, 0x41800000, v53
	v_cvt_pk_fp8_f32 v61, v57, v56 op_sel:[0,0,1]
	v_med3_f32 v56, v52, s75, v180
	v_med3_f32 v53, v53, s75, v180
	v_mov_b32_e32 v52, v145
	v_pk_fma_f32 v[54:55], v[54:55], s[40:41], v[134:135] op_sel_hi:[1,0,1]
	v_cvt_pk_fp8_f32 v52, v56, v53
	v_pk_mul_f32 v[54:55], v[54:55], v[154:155] op_sel_hi:[1,0]
	v_pk_fma_f32 v[48:49], v[48:49], s[40:41], v[128:129] op_sel_hi:[1,0,1]
	v_mul_f32_e32 v54, 0x41800000, v54
	v_pk_mul_f32 v[48:49], v[48:49], v[154:155] op_sel_hi:[1,0]
	v_mul_f32_e32 v53, 0x41800000, v55
	v_med3_f32 v54, v54, s75, v180
	v_med3_f32 v53, v53, s75, v180
	v_mul_f32_e32 v48, 0x41800000, v48
	v_mul_f32_e32 v49, 0x41800000, v49
	v_cvt_pk_fp8_f32 v52, v54, v53 op_sel:[0,0,1]
	v_med3_f32 v48, v48, s75, v180
	v_med3_f32 v49, v49, s75, v180
	v_mov_b32_e32 v53, v145
	v_pk_fma_f32 v[50:51], v[50:51], s[40:41], v[130:131] op_sel_hi:[1,0,1]
	v_cvt_pk_fp8_f32 v53, v48, v49
	v_pk_mul_f32 v[50:51], v[50:51], v[154:155] op_sel_hi:[1,0]
	v_lshlrev_b64 v[64:65], 11, v[144:145]
	v_mul_f32_e32 v50, 0x41800000, v50
	v_mul_f32_e32 v48, 0x41800000, v51
	v_med3_f32 v49, v50, s75, v180
	v_med3_f32 v48, v48, s75, v180
	v_cvt_pk_fp8_f32 v53, v49, v48 op_sel:[0,0,1]
	v_lshl_add_u64 v[48:49], s[36:37], 0, v[64:65]
	v_lshl_add_u64 v[48:49], v[48:49], 0, v[148:149]
	global_store_dwordx2 v[48:49], v[60:61], off
	global_store_dwordx2 v[48:49], v[52:53], off offset:128
.LBB0_1267:
	s_or_b64 exec, exec, s[8:9]
	v_cndmask_b32_e64 v144, -1, v187, s[6:7]
	v_cmp_lt_i32_e64 s[0:1], -1, v144
	s_and_saveexec_b64 s[6:7], s[0:1]
	s_cbranch_execz .LBB0_1269
	v_pk_fma_f32 v[44:45], v[44:45], s[40:41], v[140:141] op_sel_hi:[1,0,1]
	v_pk_fma_f32 v[46:47], v[46:47], s[40:41], v[142:143] op_sel_hi:[1,0,1]
	v_pk_mul_f32 v[44:45], v[44:45], v[152:153] op_sel_hi:[1,0]
	v_pk_mul_f32 v[46:47], v[46:47], v[152:153] op_sel_hi:[1,0]
	v_mul_f32_e32 v44, 0x41800000, v44
	v_mul_f32_e32 v45, 0x41800000, v45
	v_med3_f32 v50, v44, s75, v180
	v_med3_f32 v45, v45, s75, v180
	v_mov_b32_e32 v44, v145
	v_cvt_pk_fp8_f32 v44, v50, v45
	v_pk_fma_f32 v[40:41], v[40:41], s[40:41], v[136:137] op_sel_hi:[1,0,1]
	v_mul_f32_e32 v46, 0x41800000, v46
	v_pk_mul_f32 v[40:41], v[40:41], v[152:153] op_sel_hi:[1,0]
	v_mul_f32_e32 v45, 0x41800000, v47
	v_med3_f32 v46, v46, s75, v180
	v_med3_f32 v45, v45, s75, v180
	v_mul_f32_e32 v40, 0x41800000, v40
	v_mul_f32_e32 v41, 0x41800000, v41
	v_cvt_pk_fp8_f32 v44, v46, v45 op_sel:[0,0,1]
	v_med3_f32 v40, v40, s75, v180
	v_med3_f32 v41, v41, s75, v180
	v_mov_b32_e32 v45, v145
	v_pk_fma_f32 v[42:43], v[42:43], s[40:41], v[138:139] op_sel_hi:[1,0,1]
	v_cvt_pk_fp8_f32 v45, v40, v41
	v_pk_mul_f32 v[42:43], v[42:43], v[152:153] op_sel_hi:[1,0]
	v_pk_fma_f32 v[36:37], v[36:37], s[40:41], v[132:133] op_sel_hi:[1,0,1]
	v_mul_f32_e32 v42, 0x41800000, v42
	v_mul_f32_e32 v40, 0x41800000, v43
	v_pk_mul_f32 v[36:37], v[36:37], v[152:153] op_sel_hi:[1,0]
	v_med3_f32 v41, v42, s75, v180
	v_med3_f32 v40, v40, s75, v180
	v_mul_f32_e32 v36, 0x41800000, v36
	v_mul_f32_e32 v37, 0x41800000, v37
	v_cvt_pk_fp8_f32 v45, v41, v40 op_sel:[0,0,1]
	v_med3_f32 v40, v36, s75, v180
	v_med3_f32 v37, v37, s75, v180
	v_mov_b32_e32 v36, v145
	v_pk_fma_f32 v[38:39], v[38:39], s[40:41], v[134:135] op_sel_hi:[1,0,1]
	v_cvt_pk_fp8_f32 v36, v40, v37
	v_pk_mul_f32 v[38:39], v[38:39], v[152:153] op_sel_hi:[1,0]
	v_pk_fma_f32 v[32:33], v[32:33], s[40:41], v[128:129] op_sel_hi:[1,0,1]
	v_mul_f32_e32 v38, 0x41800000, v38
	v_pk_mul_f32 v[32:33], v[32:33], v[152:153] op_sel_hi:[1,0]
	v_mul_f32_e32 v37, 0x41800000, v39
	v_med3_f32 v38, v38, s75, v180
	v_med3_f32 v37, v37, s75, v180
	v_mul_f32_e32 v32, 0x41800000, v32
	v_mul_f32_e32 v33, 0x41800000, v33
	v_cvt_pk_fp8_f32 v36, v38, v37 op_sel:[0,0,1]
	v_med3_f32 v32, v32, s75, v180
	v_med3_f32 v33, v33, s75, v180
	v_mov_b32_e32 v37, v145
	v_pk_fma_f32 v[34:35], v[34:35], s[40:41], v[130:131] op_sel_hi:[1,0,1]
	v_cvt_pk_fp8_f32 v37, v32, v33
	v_pk_mul_f32 v[34:35], v[34:35], v[152:153] op_sel_hi:[1,0]
	v_lshlrev_b64 v[48:49], 11, v[144:145]
	v_mul_f32_e32 v34, 0x41800000, v34
	v_mul_f32_e32 v32, 0x41800000, v35
	v_med3_f32 v33, v34, s75, v180
	v_med3_f32 v32, v32, s75, v180
	v_cvt_pk_fp8_f32 v37, v33, v32 op_sel:[0,0,1]
	v_lshl_add_u64 v[32:33], s[36:37], 0, v[48:49]
	v_lshl_add_u64 v[32:33], v[32:33], 0, v[148:149]
	global_store_dwordx2 v[32:33], v[44:45], off
	global_store_dwordx2 v[32:33], v[36:37], off offset:128
.LBB0_1269:
	s_or_b64 exec, exec, s[6:7]
	v_cndmask_b32_e64 v144, -1, v186, s[4:5]
	v_cmp_lt_i32_e64 s[0:1], -1, v144
	s_and_saveexec_b64 s[4:5], s[0:1]
	s_cbranch_execz .LBB0_1271
	v_pk_fma_f32 v[28:29], v[28:29], s[40:41], v[140:141] op_sel_hi:[1,0,1]
	v_pk_fma_f32 v[30:31], v[30:31], s[40:41], v[142:143] op_sel_hi:[1,0,1]
	v_pk_mul_f32 v[28:29], v[28:29], v[150:151] op_sel_hi:[1,0]
	v_pk_mul_f32 v[30:31], v[30:31], v[150:151] op_sel_hi:[1,0]
	v_mul_f32_e32 v28, 0x41800000, v28
	v_mul_f32_e32 v29, 0x41800000, v29
	v_med3_f32 v34, v28, s75, v180
	v_med3_f32 v29, v29, s75, v180
	v_mov_b32_e32 v28, v145
	v_cvt_pk_fp8_f32 v28, v34, v29
	v_pk_fma_f32 v[24:25], v[24:25], s[40:41], v[136:137] op_sel_hi:[1,0,1]
	v_mul_f32_e32 v30, 0x41800000, v30
	v_pk_mul_f32 v[24:25], v[24:25], v[150:151] op_sel_hi:[1,0]
	v_mul_f32_e32 v29, 0x41800000, v31
	v_med3_f32 v30, v30, s75, v180
	v_med3_f32 v29, v29, s75, v180
	v_mul_f32_e32 v24, 0x41800000, v24
	v_mul_f32_e32 v25, 0x41800000, v25
	v_cvt_pk_fp8_f32 v28, v30, v29 op_sel:[0,0,1]
	v_med3_f32 v24, v24, s75, v180
	v_med3_f32 v25, v25, s75, v180
	v_mov_b32_e32 v29, v145
	v_pk_fma_f32 v[26:27], v[26:27], s[40:41], v[138:139] op_sel_hi:[1,0,1]
	v_cvt_pk_fp8_f32 v29, v24, v25
	v_pk_mul_f32 v[26:27], v[26:27], v[150:151] op_sel_hi:[1,0]
	v_pk_fma_f32 v[20:21], v[20:21], s[40:41], v[132:133] op_sel_hi:[1,0,1]
	v_mul_f32_e32 v26, 0x41800000, v26
	v_mul_f32_e32 v24, 0x41800000, v27
	v_pk_mul_f32 v[20:21], v[20:21], v[150:151] op_sel_hi:[1,0]
	v_med3_f32 v25, v26, s75, v180
	v_med3_f32 v24, v24, s75, v180
	v_mul_f32_e32 v20, 0x41800000, v20
	v_mul_f32_e32 v21, 0x41800000, v21
	v_cvt_pk_fp8_f32 v29, v25, v24 op_sel:[0,0,1]
	v_med3_f32 v24, v20, s75, v180
	v_med3_f32 v21, v21, s75, v180
	v_mov_b32_e32 v20, v145
	v_pk_fma_f32 v[22:23], v[22:23], s[40:41], v[134:135] op_sel_hi:[1,0,1]
	v_cvt_pk_fp8_f32 v20, v24, v21
	v_pk_mul_f32 v[22:23], v[22:23], v[150:151] op_sel_hi:[1,0]
	v_pk_fma_f32 v[16:17], v[16:17], s[40:41], v[128:129] op_sel_hi:[1,0,1]
	v_mul_f32_e32 v22, 0x41800000, v22
	v_pk_mul_f32 v[16:17], v[16:17], v[150:151] op_sel_hi:[1,0]
	v_mul_f32_e32 v21, 0x41800000, v23
	v_med3_f32 v22, v22, s75, v180
	v_med3_f32 v21, v21, s75, v180
	v_mul_f32_e32 v16, 0x41800000, v16
	v_mul_f32_e32 v17, 0x41800000, v17
	v_cvt_pk_fp8_f32 v20, v22, v21 op_sel:[0,0,1]
	v_med3_f32 v16, v16, s75, v180
	v_med3_f32 v17, v17, s75, v180
	v_mov_b32_e32 v21, v145
	v_pk_fma_f32 v[18:19], v[18:19], s[40:41], v[130:131] op_sel_hi:[1,0,1]
	v_cvt_pk_fp8_f32 v21, v16, v17
	v_pk_mul_f32 v[18:19], v[18:19], v[150:151] op_sel_hi:[1,0]
	v_lshlrev_b64 v[32:33], 11, v[144:145]
	v_mul_f32_e32 v18, 0x41800000, v18
	v_mul_f32_e32 v16, 0x41800000, v19
	v_med3_f32 v17, v18, s75, v180
	v_med3_f32 v16, v16, s75, v180
	v_cvt_pk_fp8_f32 v21, v17, v16 op_sel:[0,0,1]
	v_lshl_add_u64 v[16:17], s[36:37], 0, v[32:33]
	v_lshl_add_u64 v[16:17], v[16:17], 0, v[148:149]
	global_store_dwordx2 v[16:17], v[28:29], off
	global_store_dwordx2 v[16:17], v[20:21], off offset:128
.LBB0_1271:
	s_or_b64 exec, exec, s[4:5]
	v_cndmask_b32_e32 v144, -1, v147, vcc
	v_cmp_lt_i32_e32 vcc, -1, v144
	s_and_saveexec_b64 s[0:1], vcc
	s_cbranch_execz .LBB0_1273
	v_pk_fma_f32 v[12:13], v[12:13], s[40:41], v[140:141] op_sel_hi:[1,0,1]
	v_pk_fma_f32 v[14:15], v[14:15], s[40:41], v[142:143] op_sel_hi:[1,0,1]
	v_pk_mul_f32 v[12:13], v[12:13], v[146:147] op_sel_hi:[1,0]
	v_pk_mul_f32 v[14:15], v[14:15], v[146:147] op_sel_hi:[1,0]
	v_mul_f32_e32 v12, 0x41800000, v12
	v_mul_f32_e32 v13, 0x41800000, v13
	v_med3_f32 v18, v12, s75, v180
	v_med3_f32 v13, v13, s75, v180
	v_mov_b32_e32 v12, v145
	v_cvt_pk_fp8_f32 v12, v18, v13
	v_pk_fma_f32 v[8:9], v[8:9], s[40:41], v[136:137] op_sel_hi:[1,0,1]
	v_mul_f32_e32 v14, 0x41800000, v14
	v_pk_mul_f32 v[8:9], v[8:9], v[146:147] op_sel_hi:[1,0]
	v_mul_f32_e32 v13, 0x41800000, v15
	v_med3_f32 v14, v14, s75, v180
	v_med3_f32 v13, v13, s75, v180
	v_mul_f32_e32 v8, 0x41800000, v8
	v_mul_f32_e32 v9, 0x41800000, v9
	v_cvt_pk_fp8_f32 v12, v14, v13 op_sel:[0,0,1]
	v_med3_f32 v8, v8, s75, v180
	v_med3_f32 v9, v9, s75, v180
	v_mov_b32_e32 v13, v145
	v_pk_fma_f32 v[10:11], v[10:11], s[40:41], v[138:139] op_sel_hi:[1,0,1]
	v_cvt_pk_fp8_f32 v13, v8, v9
	v_pk_mul_f32 v[10:11], v[10:11], v[146:147] op_sel_hi:[1,0]
	v_pk_fma_f32 v[4:5], v[4:5], s[40:41], v[132:133] op_sel_hi:[1,0,1]
	v_mul_f32_e32 v10, 0x41800000, v10
	v_mul_f32_e32 v8, 0x41800000, v11
	v_pk_mul_f32 v[4:5], v[4:5], v[146:147] op_sel_hi:[1,0]
	v_med3_f32 v9, v10, s75, v180
	v_med3_f32 v8, v8, s75, v180
	v_mul_f32_e32 v4, 0x41800000, v4
	v_mul_f32_e32 v5, 0x41800000, v5
	v_cvt_pk_fp8_f32 v13, v9, v8 op_sel:[0,0,1]
	v_med3_f32 v8, v4, s75, v180
	v_med3_f32 v5, v5, s75, v180
	v_mov_b32_e32 v4, v145
	v_pk_fma_f32 v[6:7], v[6:7], s[40:41], v[134:135] op_sel_hi:[1,0,1]
	v_cvt_pk_fp8_f32 v4, v8, v5
	v_pk_mul_f32 v[6:7], v[6:7], v[146:147] op_sel_hi:[1,0]
	v_pk_fma_f32 v[0:1], v[0:1], s[40:41], v[128:129] op_sel_hi:[1,0,1]
	v_mul_f32_e32 v6, 0x41800000, v6
	v_pk_mul_f32 v[0:1], v[0:1], v[146:147] op_sel_hi:[1,0]
	v_mul_f32_e32 v5, 0x41800000, v7
	v_med3_f32 v6, v6, s75, v180
	v_med3_f32 v5, v5, s75, v180
	v_mul_f32_e32 v0, 0x41800000, v0
	v_mul_f32_e32 v1, 0x41800000, v1
	v_cvt_pk_fp8_f32 v4, v6, v5 op_sel:[0,0,1]
	v_med3_f32 v0, v0, s75, v180
	v_med3_f32 v1, v1, s75, v180
	v_mov_b32_e32 v5, v145
	v_pk_fma_f32 v[2:3], v[2:3], s[40:41], v[130:131] op_sel_hi:[1,0,1]
	v_cvt_pk_fp8_f32 v5, v0, v1
	v_pk_mul_f32 v[2:3], v[2:3], v[146:147] op_sel_hi:[1,0]
	v_lshlrev_b64 v[16:17], 11, v[144:145]
	v_mul_f32_e32 v2, 0x41800000, v2
	v_mul_f32_e32 v0, 0x41800000, v3
	v_med3_f32 v1, v2, s75, v180
	v_med3_f32 v0, v0, s75, v180
	v_cvt_pk_fp8_f32 v5, v1, v0 op_sel:[0,0,1]
	v_lshl_add_u64 v[0:1], s[36:37], 0, v[16:17]
	v_lshl_add_u64 v[0:1], v[0:1], 0, v[148:149]
	global_store_dwordx2 v[0:1], v[12:13], off
	global_store_dwordx2 v[0:1], v[4:5], off offset:128
